# opt8: software-pipelined the 8 MoE weight conversion loops (next item's 16 loads issued before current item's LDS read/convert/store; flat->global loads); bit-identical
# baseline (speedup 1.0000x reference)
.LBB0_294:
	s_ashr_i32 s2, s14, 31
	s_lshr_b32 s2, s2, 23
	s_add_i32 s2, s14, s2
	s_ashr_i32 s4, s2, 9
	s_and_b32 s2, s2, 0xfe00
	s_sub_i32 s2, s14, s2
	s_sext_i32_i16 s3, s2
	s_bfe_u32 s3, s3, 0x4001b
	s_add_i32 s3, s2, s3
	s_sext_i32_i16 s5, s3
	s_and_b32 s3, s3, 0xfff0
	s_sub_i32 s2, s2, s3
	s_sext_i32_i16 s18, s2
	s_lshl_b32 s2, s5, 2
	s_ashr_i32 s5, s4, 31
	s_andn2_b32 s2, s2, 63
	s_lshl_b32 s6, s18, 6
	s_lshl_b64 s[4:5], s[4:5], 23
	s_add_u32 s7, s15, s4
	s_addc_u32 s19, s16, s5
	s_ashr_i32 s3, s2, 31
	s_lshl_b64 s[20:21], s[2:3], 12
	s_add_u32 s22, s7, s20
	s_addc_u32 s19, s19, s21
	s_ashr_i32 s7, s6, 31
	s_lshl_b64 s[20:21], s[6:7], 2
	s_add_u32 s20, s22, s20
	s_addc_u32 s21, s19, s21
	v_lshl_add_u64 v[0:1], s[20:21], 0, v[96:97]
	v_lshl_add_u64 v[2:3], v[0:1], 0, v[60:61]
	global_load_dwordx4 v[116:119], v[2:3], off nt
	v_lshl_add_u64 v[2:3], v[0:1], 0, v[62:63]
	global_load_dwordx4 v[56:59], v[2:3], off nt
	v_lshl_add_u64 v[2:3], v[0:1], 0, v[64:65]
	global_load_dwordx4 v[52:55], v[2:3], off nt
	v_lshl_add_u64 v[2:3], v[0:1], 0, v[66:67]
	global_load_dwordx4 v[48:51], v[2:3], off nt
	v_lshl_add_u64 v[2:3], v[0:1], 0, v[68:69]
	global_load_dwordx4 v[44:47], v[2:3], off nt
	v_lshl_add_u64 v[2:3], v[0:1], 0, v[70:71]
	global_load_dwordx4 v[40:43], v[2:3], off nt
	v_lshl_add_u64 v[2:3], v[0:1], 0, v[72:73]
	global_load_dwordx4 v[36:39], v[2:3], off nt
	v_lshl_add_u64 v[2:3], v[0:1], 0, v[74:75]
	global_load_dwordx4 v[32:35], v[2:3], off nt
	v_lshl_add_u64 v[2:3], v[0:1], 0, v[76:77]
	global_load_dwordx4 v[28:31], v[2:3], off nt
	v_lshl_add_u64 v[2:3], v[0:1], 0, v[78:79]
	global_load_dwordx4 v[24:27], v[2:3], off nt
	v_lshl_add_u64 v[2:3], v[0:1], 0, v[80:81]
	global_load_dwordx4 v[20:23], v[2:3], off nt
	v_lshl_add_u64 v[2:3], v[0:1], 0, v[82:83]
	global_load_dwordx4 v[16:19], v[2:3], off nt
	v_lshl_add_u64 v[2:3], v[0:1], 0, v[84:85]
	global_load_dwordx4 v[12:15], v[2:3], off nt
	v_lshl_add_u64 v[2:3], v[0:1], 0, v[86:87]
	global_load_dwordx4 v[8:11], v[2:3], off nt
	v_lshl_add_u64 v[2:3], v[0:1], 0, v[88:89]
	global_load_dwordx4 v[4:7], v[2:3], off nt
	v_lshl_add_u64 v[0:1], v[0:1], 0, v[90:91]
	global_load_dwordx4 v[0:3], v[0:1], off nt
	v_add_u32_e32 v111, 0x410, v114
	s_lshl_b32 s7, s18, 7
	s_and_b32 s6, s6, 64
	s_or_b32 s6, s6, s7
	s_bitset1_b32 s6, 7
	s_ashr_i32 s7, s6, 31
	s_add_u32 s18, s23, s4
	s_addc_u32 s19, s24, s5
	s_lshl_b64 s[4:5], s[6:7], 12
	s_add_u32 s4, s18, s4
	s_addc_u32 s5, s19, s5
	s_lshl_b64 s[2:3], s[2:3], 1
	s_add_u32 s2, s4, s2
	s_addc_u32 s3, s5, s3
.Lcvp_0_loop:
	s_waitcnt vmcnt(0) lgkmcnt(0)
	ds_write2_b32 v114, v116, v117 offset1:1
	ds_write2_b32 v114, v118, v119 offset0:2 offset1:3
	ds_write2_b32 v111, v56, v57 offset1:1
	v_add_u32_e32 v56, 0x418, v114
	ds_write2_b32 v56, v58, v59 offset1:1
	v_add_u32_e32 v56, 0x820, v114
	ds_write2_b32 v56, v52, v53 offset1:1
	v_add_u32_e32 v52, 0x828, v114
	ds_write2_b32 v52, v54, v55 offset1:1
	v_add_u32_e32 v52, 0xc30, v114
	ds_write2_b32 v52, v48, v49 offset1:1
	v_add_u32_e32 v48, 0xc38, v114
	ds_write2_b32 v48, v50, v51 offset1:1
	v_add_u32_e32 v48, 0x1040, v114
	ds_write2_b32 v48, v44, v45 offset1:1
	v_add_u32_e32 v44, 0x1048, v114
	ds_write2_b32 v44, v46, v47 offset1:1
	v_add_u32_e32 v44, 0x1450, v114
	ds_write2_b32 v44, v40, v41 offset1:1
	v_add_u32_e32 v40, 0x1458, v114
	ds_write2_b32 v40, v42, v43 offset1:1
	v_add_u32_e32 v40, 0x1860, v114
	ds_write2_b32 v40, v36, v37 offset1:1
	v_add_u32_e32 v36, 0x1868, v114
	ds_write2_b32 v36, v38, v39 offset1:1
	v_add_u32_e32 v36, 0x1c70, v114
	ds_write2_b32 v36, v32, v33 offset1:1
	v_add_u32_e32 v32, 0x1c78, v114
	ds_write2_b32 v32, v34, v35 offset1:1
	v_add_u32_e32 v32, 0x2080, v114
	ds_write2_b32 v32, v28, v29 offset1:1
	v_add_u32_e32 v28, 0x2088, v114
	ds_write2_b32 v28, v30, v31 offset1:1
	v_add_u32_e32 v28, 0x2490, v114
	ds_write2_b32 v28, v24, v25 offset1:1
	v_add_u32_e32 v24, 0x2498, v114
	ds_write2_b32 v24, v26, v27 offset1:1
	v_add_u32_e32 v24, 0x28a0, v114
	ds_write2_b32 v24, v20, v21 offset1:1
	v_add_u32_e32 v20, 0x28a8, v114
	ds_write2_b32 v20, v22, v23 offset1:1
	v_add_u32_e32 v20, 0x2cb0, v114
	ds_write2_b32 v20, v16, v17 offset1:1
	v_add_u32_e32 v16, 0x2cb8, v114
	ds_write2_b32 v16, v18, v19 offset1:1
	v_add_u32_e32 v16, 0x30c0, v114
	ds_write2_b32 v16, v12, v13 offset1:1
	v_add_u32_e32 v12, 0x30c8, v114
	ds_write2_b32 v12, v14, v15 offset1:1
	v_add_u32_e32 v12, 0x34d0, v114
	ds_write2_b32 v12, v8, v9 offset1:1
	v_add_u32_e32 v8, 0x34d8, v114
	ds_write2_b32 v8, v10, v11 offset1:1
	v_add_u32_e32 v8, 0x38e0, v114
	ds_write2_b32 v8, v4, v5 offset1:1
	v_add_u32_e32 v4, 0x38e8, v114
	ds_write2_b32 v4, v6, v7 offset1:1
	v_add_u32_e32 v4, 0x3cf0, v114
	ds_write2_b32 v4, v0, v1 offset1:1
	v_add_u32_e32 v0, 0x3cf8, v114
	ds_write2_b32 v0, v2, v3 offset1:1
	v_mov_b32_e32 v111, v97
	v_lshl_add_u64 v[174:175], s[2:3], 0, v[110:111]
	s_add_i32 s14, s14, s80
	s_cmpk_lt_i32 s14, 0x1000
	s_cbranch_scc0 .Lcvp_0_skip
	s_ashr_i32 s2, s14, 31
	s_lshr_b32 s2, s2, 23
	s_add_i32 s2, s14, s2
	s_ashr_i32 s4, s2, 9
	s_and_b32 s2, s2, 0xfe00
	s_sub_i32 s2, s14, s2
	s_sext_i32_i16 s3, s2
	s_bfe_u32 s3, s3, 0x4001b
	s_add_i32 s3, s2, s3
	s_sext_i32_i16 s5, s3
	s_and_b32 s3, s3, 0xfff0
	s_sub_i32 s2, s2, s3
	s_sext_i32_i16 s18, s2
	s_lshl_b32 s2, s5, 2
	s_ashr_i32 s5, s4, 31
	s_andn2_b32 s2, s2, 63
	s_lshl_b32 s6, s18, 6
	s_lshl_b64 s[4:5], s[4:5], 23
	s_add_u32 s7, s15, s4
	s_addc_u32 s19, s16, s5
	s_ashr_i32 s3, s2, 31
	s_lshl_b64 s[20:21], s[2:3], 12
	s_add_u32 s22, s7, s20
	s_addc_u32 s19, s19, s21
	s_ashr_i32 s7, s6, 31
	s_lshl_b64 s[20:21], s[6:7], 2
	s_add_u32 s20, s22, s20
	s_addc_u32 s21, s19, s21
	v_lshl_add_u64 v[0:1], s[20:21], 0, v[96:97]
	v_lshl_add_u64 v[2:3], v[0:1], 0, v[60:61]
	global_load_dwordx4 v[116:119], v[2:3], off nt
	v_lshl_add_u64 v[2:3], v[0:1], 0, v[62:63]
	global_load_dwordx4 v[56:59], v[2:3], off nt
	v_lshl_add_u64 v[2:3], v[0:1], 0, v[64:65]
	global_load_dwordx4 v[52:55], v[2:3], off nt
	v_lshl_add_u64 v[2:3], v[0:1], 0, v[66:67]
	global_load_dwordx4 v[48:51], v[2:3], off nt
	v_lshl_add_u64 v[2:3], v[0:1], 0, v[68:69]
	global_load_dwordx4 v[44:47], v[2:3], off nt
	v_lshl_add_u64 v[2:3], v[0:1], 0, v[70:71]
	global_load_dwordx4 v[40:43], v[2:3], off nt
	v_lshl_add_u64 v[2:3], v[0:1], 0, v[72:73]
	global_load_dwordx4 v[36:39], v[2:3], off nt
	v_lshl_add_u64 v[2:3], v[0:1], 0, v[74:75]
	global_load_dwordx4 v[32:35], v[2:3], off nt
	v_lshl_add_u64 v[2:3], v[0:1], 0, v[76:77]
	global_load_dwordx4 v[28:31], v[2:3], off nt
	v_lshl_add_u64 v[2:3], v[0:1], 0, v[78:79]
	global_load_dwordx4 v[24:27], v[2:3], off nt
	v_lshl_add_u64 v[2:3], v[0:1], 0, v[80:81]
	global_load_dwordx4 v[20:23], v[2:3], off nt
	v_lshl_add_u64 v[2:3], v[0:1], 0, v[82:83]
	global_load_dwordx4 v[16:19], v[2:3], off nt
	v_lshl_add_u64 v[2:3], v[0:1], 0, v[84:85]
	global_load_dwordx4 v[12:15], v[2:3], off nt
	v_lshl_add_u64 v[2:3], v[0:1], 0, v[86:87]
	global_load_dwordx4 v[8:11], v[2:3], off nt
	v_lshl_add_u64 v[2:3], v[0:1], 0, v[88:89]
	global_load_dwordx4 v[4:7], v[2:3], off nt
	v_lshl_add_u64 v[0:1], v[0:1], 0, v[90:91]
	global_load_dwordx4 v[0:3], v[0:1], off nt
	v_add_u32_e32 v111, 0x410, v114
	s_lshl_b32 s7, s18, 7
	s_and_b32 s6, s6, 64
	s_or_b32 s6, s6, s7
	s_bitset1_b32 s6, 7
	s_ashr_i32 s7, s6, 31
	s_add_u32 s18, s23, s4
	s_addc_u32 s19, s24, s5
	s_lshl_b64 s[4:5], s[6:7], 12
	s_add_u32 s4, s18, s4
	s_addc_u32 s5, s19, s5
	s_lshl_b64 s[2:3], s[2:3], 1
	s_add_u32 s2, s4, s2
	s_addc_u32 s3, s5, s3
.Lcvp_0_skip:
	s_waitcnt lgkmcnt(0)
	ds_read2_b32 v[176:177], v113 offset0:65 offset1:73
	ds_read2_b32 v[178:179], v113 offset1:8
	ds_read2_b32 v[180:181], v113 offset0:130 offset1:138
	ds_read2_b32 v[182:183], v113 offset0:195 offset1:203
	v_lshl_add_u64 v[192:193], v[174:175], 0, v[92:93]
	s_waitcnt lgkmcnt(2)
	v_cvt_pk_bf16_f32 v170, v178, v176
	v_add_u32_e32 v176, 0x400, v113
	ds_read2_b32 v[184:185], v176 offset0:4 offset1:12
	ds_read2_b32 v[186:187], v176 offset0:69 offset1:77
	ds_read2_b32 v[188:189], v176 offset0:134 offset1:142
	ds_read2_b32 v[190:191], v176 offset0:199 offset1:207
	s_waitcnt lgkmcnt(4)
	v_cvt_pk_bf16_f32 v171, v180, v182
	v_lshl_add_u64 v[194:195], v[174:175], 0, v[98:99]
	s_waitcnt lgkmcnt(2)
	v_cvt_pk_bf16_f32 v172, v184, v186
	s_waitcnt lgkmcnt(0)
	v_cvt_pk_bf16_f32 v173, v188, v190
	global_store_dwordx4 v[192:193], v[170:173], off
	s_nop 1
	v_cvt_pk_bf16_f32 v170, v179, v177
	v_cvt_pk_bf16_f32 v171, v181, v183
	v_cvt_pk_bf16_f32 v172, v185, v187
	v_cvt_pk_bf16_f32 v173, v189, v191
	v_lshl_add_u64 v[178:179], v[174:175], 0, v[94:95]
	global_store_dwordx4 v[178:179], v[170:173], off
	ds_read2_b32 v[178:179], v113 offset0:81 offset1:89
	ds_read2_b32 v[180:181], v113 offset0:16 offset1:24
	ds_read2_b32 v[182:183], v113 offset0:146 offset1:154
	ds_read2_b32 v[184:185], v113 offset0:211 offset1:219
	ds_read2_b32 v[186:187], v176 offset0:20 offset1:28
	ds_read2_b32 v[188:189], v176 offset0:85 offset1:93
	ds_read2_b32 v[190:191], v176 offset0:150 offset1:158
	ds_read2_b32 v[192:193], v176 offset0:215 offset1:223
	s_waitcnt lgkmcnt(6)
	v_cvt_pk_bf16_f32 v170, v180, v178
	s_waitcnt lgkmcnt(4)
	v_cvt_pk_bf16_f32 v171, v182, v184
	s_waitcnt lgkmcnt(2)
	v_cvt_pk_bf16_f32 v172, v186, v188
	s_waitcnt lgkmcnt(0)
	v_cvt_pk_bf16_f32 v173, v190, v192
	global_store_dwordx4 v[194:195], v[170:173], off
	v_lshl_add_u64 v[194:195], v[174:175], 0, v[102:103]
	s_nop 0
	v_cvt_pk_bf16_f32 v170, v181, v179
	v_cvt_pk_bf16_f32 v171, v183, v185
	v_cvt_pk_bf16_f32 v172, v187, v189
	v_cvt_pk_bf16_f32 v173, v191, v193
	v_lshl_add_u64 v[178:179], v[174:175], 0, v[100:101]
	global_store_dwordx4 v[178:179], v[170:173], off
	ds_read2_b32 v[178:179], v113 offset0:32 offset1:40
	ds_read2_b32 v[180:181], v113 offset0:97 offset1:105
	ds_read2_b32 v[182:183], v113 offset0:162 offset1:170
	ds_read2_b32 v[184:185], v113 offset0:227 offset1:235
	ds_read2_b32 v[186:187], v176 offset0:36 offset1:44
	ds_read2_b32 v[188:189], v176 offset0:101 offset1:109
	ds_read2_b32 v[190:191], v176 offset0:166 offset1:174
	ds_read2_b32 v[192:193], v176 offset0:231 offset1:239
	s_waitcnt lgkmcnt(6)
	v_cvt_pk_bf16_f32 v170, v178, v180
	s_waitcnt lgkmcnt(4)
	v_cvt_pk_bf16_f32 v171, v182, v184
	s_waitcnt lgkmcnt(2)
	v_cvt_pk_bf16_f32 v172, v186, v188
	s_waitcnt lgkmcnt(0)
	v_cvt_pk_bf16_f32 v173, v190, v192
	global_store_dwordx4 v[194:195], v[170:173], off
	s_nop 1
	v_cvt_pk_bf16_f32 v170, v179, v181
	v_cvt_pk_bf16_f32 v171, v183, v185
	v_cvt_pk_bf16_f32 v172, v187, v189
	v_cvt_pk_bf16_f32 v173, v191, v193
	v_lshl_add_u64 v[178:179], v[174:175], 0, v[104:105]
	global_store_dwordx4 v[178:179], v[170:173], off
	ds_read2_b32 v[178:179], v113 offset0:48 offset1:56
	ds_read2_b32 v[180:181], v113 offset0:113 offset1:121
	ds_read2_b32 v[182:183], v113 offset0:178 offset1:186
	ds_read2_b32 v[184:185], v113 offset0:243 offset1:251
	ds_read2_b32 v[186:187], v176 offset0:52 offset1:60
	ds_read2_b32 v[188:189], v176 offset0:117 offset1:125
	ds_read2_b32 v[190:191], v176 offset0:182 offset1:190
	ds_read2_b32 v[176:177], v176 offset0:247 offset1:255
	v_lshl_add_u64 v[192:193], v[174:175], 0, v[106:107]
	s_waitcnt lgkmcnt(6)
	v_cvt_pk_bf16_f32 v170, v178, v180
	s_waitcnt lgkmcnt(4)
	v_cvt_pk_bf16_f32 v171, v182, v184
	s_waitcnt lgkmcnt(2)
	v_cvt_pk_bf16_f32 v172, v186, v188
	s_waitcnt lgkmcnt(0)
	v_cvt_pk_bf16_f32 v173, v190, v176
	global_store_dwordx4 v[192:193], v[170:173], off
	v_lshl_add_u64 v[174:175], v[174:175], 0, v[108:109]
	s_nop 0
	v_cvt_pk_bf16_f32 v170, v179, v181
	v_cvt_pk_bf16_f32 v171, v183, v185
	v_cvt_pk_bf16_f32 v172, v187, v189
	v_cvt_pk_bf16_f32 v173, v191, v177
	global_store_dwordx4 v[174:175], v[170:173], off
	s_waitcnt lgkmcnt(0)
	s_cmpk_lt_i32 s14, 0x1000
	s_cbranch_scc1 .Lcvp_0_loop

.LBB0_297:
	s_ashr_i32 s2, s12, 31
	s_lshr_b32 s2, s2, 23
	s_add_i32 s2, s12, s2
	s_ashr_i32 s4, s2, 9
	s_and_b32 s2, s2, 0xfe00
	s_sub_i32 s2, s12, s2
	s_sext_i32_i16 s3, s2
	s_bfe_u32 s3, s3, 0x4001b
	s_add_i32 s3, s2, s3
	s_sext_i32_i16 s5, s3
	s_and_b32 s3, s3, 0xfff0
	s_sub_i32 s2, s2, s3
	s_sext_i32_i16 s13, s2
	s_lshl_b32 s2, s5, 2
	s_ashr_i32 s5, s4, 31
	s_andn2_b32 s2, s2, 63
	s_lshl_b32 s6, s13, 6
	s_lshl_b64 s[4:5], s[4:5], 23
	s_add_u32 s7, s14, s4
	s_addc_u32 s16, s15, s5
	s_ashr_i32 s3, s2, 31
	s_lshl_b64 s[18:19], s[2:3], 12
	s_add_u32 s20, s7, s18
	s_addc_u32 s16, s16, s19
	s_ashr_i32 s7, s6, 31
	s_lshl_b64 s[18:19], s[6:7], 2
	s_add_u32 s18, s20, s18
	s_addc_u32 s19, s16, s19
	v_lshl_add_u64 v[0:1], s[18:19], 0, v[96:97]
	v_lshl_add_u64 v[2:3], v[0:1], 0, v[60:61]
	global_load_dwordx4 v[114:117], v[2:3], off nt
	v_lshl_add_u64 v[2:3], v[0:1], 0, v[62:63]
	global_load_dwordx4 v[56:59], v[2:3], off nt
	v_lshl_add_u64 v[2:3], v[0:1], 0, v[64:65]
	global_load_dwordx4 v[52:55], v[2:3], off nt
	v_lshl_add_u64 v[2:3], v[0:1], 0, v[66:67]
	global_load_dwordx4 v[48:51], v[2:3], off nt
	v_lshl_add_u64 v[2:3], v[0:1], 0, v[68:69]
	global_load_dwordx4 v[44:47], v[2:3], off nt
	v_lshl_add_u64 v[2:3], v[0:1], 0, v[70:71]
	global_load_dwordx4 v[40:43], v[2:3], off nt
	v_lshl_add_u64 v[2:3], v[0:1], 0, v[72:73]
	global_load_dwordx4 v[36:39], v[2:3], off nt
	v_lshl_add_u64 v[2:3], v[0:1], 0, v[74:75]
	global_load_dwordx4 v[32:35], v[2:3], off nt
	v_lshl_add_u64 v[2:3], v[0:1], 0, v[76:77]
	global_load_dwordx4 v[28:31], v[2:3], off nt
	v_lshl_add_u64 v[2:3], v[0:1], 0, v[78:79]
	global_load_dwordx4 v[24:27], v[2:3], off nt
	v_lshl_add_u64 v[2:3], v[0:1], 0, v[80:81]
	global_load_dwordx4 v[20:23], v[2:3], off nt
	v_lshl_add_u64 v[2:3], v[0:1], 0, v[82:83]
	global_load_dwordx4 v[16:19], v[2:3], off nt
	v_lshl_add_u64 v[2:3], v[0:1], 0, v[84:85]
	global_load_dwordx4 v[12:15], v[2:3], off nt
	v_lshl_add_u64 v[2:3], v[0:1], 0, v[86:87]
	global_load_dwordx4 v[8:11], v[2:3], off nt
	v_lshl_add_u64 v[2:3], v[0:1], 0, v[88:89]
	global_load_dwordx4 v[4:7], v[2:3], off nt
	v_lshl_add_u64 v[0:1], v[0:1], 0, v[90:91]
	global_load_dwordx4 v[0:3], v[0:1], off nt
	v_add_u32_e32 v111, 0x410, v113
	s_lshl_b32 s7, s13, 7
	s_and_b32 s6, s6, 64
	s_or_b32 s6, s6, s7
	s_bitset1_b32 s6, 7
	s_ashr_i32 s7, s6, 31
	s_add_u32 s13, s21, s4
	s_addc_u32 s16, s22, s5
	s_lshl_b64 s[4:5], s[6:7], 12
	s_add_u32 s4, s13, s4
	s_addc_u32 s5, s16, s5
	s_lshl_b64 s[2:3], s[2:3], 1
	s_add_u32 s2, s4, s2
	s_addc_u32 s3, s5, s3
.Lcvp_1_loop:
	s_waitcnt vmcnt(0) lgkmcnt(0)
	ds_write2_b32 v113, v114, v115 offset1:1
	ds_write2_b32 v113, v116, v117 offset0:2 offset1:3
	ds_write2_b32 v111, v56, v57 offset1:1
	v_add_u32_e32 v56, 0x418, v113
	ds_write2_b32 v56, v58, v59 offset1:1
	v_add_u32_e32 v56, 0x820, v113
	ds_write2_b32 v56, v52, v53 offset1:1
	v_add_u32_e32 v52, 0x828, v113
	ds_write2_b32 v52, v54, v55 offset1:1
	v_add_u32_e32 v52, 0xc30, v113
	ds_write2_b32 v52, v48, v49 offset1:1
	v_add_u32_e32 v48, 0xc38, v113
	ds_write2_b32 v48, v50, v51 offset1:1
	v_add_u32_e32 v48, 0x1040, v113
	ds_write2_b32 v48, v44, v45 offset1:1
	v_add_u32_e32 v44, 0x1048, v113
	ds_write2_b32 v44, v46, v47 offset1:1
	v_add_u32_e32 v44, 0x1450, v113
	ds_write2_b32 v44, v40, v41 offset1:1
	v_add_u32_e32 v40, 0x1458, v113
	ds_write2_b32 v40, v42, v43 offset1:1
	v_add_u32_e32 v40, 0x1860, v113
	ds_write2_b32 v40, v36, v37 offset1:1
	v_add_u32_e32 v36, 0x1868, v113
	ds_write2_b32 v36, v38, v39 offset1:1
	v_add_u32_e32 v36, 0x1c70, v113
	ds_write2_b32 v36, v32, v33 offset1:1
	v_add_u32_e32 v32, 0x1c78, v113
	ds_write2_b32 v32, v34, v35 offset1:1
	v_add_u32_e32 v32, 0x2080, v113
	ds_write2_b32 v32, v28, v29 offset1:1
	v_add_u32_e32 v28, 0x2088, v113
	ds_write2_b32 v28, v30, v31 offset1:1
	v_add_u32_e32 v28, 0x2490, v113
	ds_write2_b32 v28, v24, v25 offset1:1
	v_add_u32_e32 v24, 0x2498, v113
	ds_write2_b32 v24, v26, v27 offset1:1
	v_add_u32_e32 v24, 0x28a0, v113
	ds_write2_b32 v24, v20, v21 offset1:1
	v_add_u32_e32 v20, 0x28a8, v113
	ds_write2_b32 v20, v22, v23 offset1:1
	v_add_u32_e32 v20, 0x2cb0, v113
	ds_write2_b32 v20, v16, v17 offset1:1
	v_add_u32_e32 v16, 0x2cb8, v113
	ds_write2_b32 v16, v18, v19 offset1:1
	v_add_u32_e32 v16, 0x30c0, v113
	ds_write2_b32 v16, v12, v13 offset1:1
	v_add_u32_e32 v12, 0x30c8, v113
	ds_write2_b32 v12, v14, v15 offset1:1
	v_add_u32_e32 v12, 0x34d0, v113
	ds_write2_b32 v12, v8, v9 offset1:1
	v_add_u32_e32 v8, 0x34d8, v113
	ds_write2_b32 v8, v10, v11 offset1:1
	v_add_u32_e32 v8, 0x38e0, v113
	ds_write2_b32 v8, v4, v5 offset1:1
	v_add_u32_e32 v4, 0x38e8, v113
	ds_write2_b32 v4, v6, v7 offset1:1
	v_add_u32_e32 v4, 0x3cf0, v113
	ds_write2_b32 v4, v0, v1 offset1:1
	v_add_u32_e32 v0, 0x3cf8, v113
	ds_write2_b32 v0, v2, v3 offset1:1
	v_mov_b32_e32 v111, v97
	v_lshl_add_u64 v[174:175], s[2:3], 0, v[110:111]
	s_add_i32 s12, s12, s80
	s_cmpk_lt_i32 s12, 0x1000
	s_cbranch_scc0 .Lcvp_1_skip
	s_ashr_i32 s2, s12, 31
	s_lshr_b32 s2, s2, 23
	s_add_i32 s2, s12, s2
	s_ashr_i32 s4, s2, 9
	s_and_b32 s2, s2, 0xfe00
	s_sub_i32 s2, s12, s2
	s_sext_i32_i16 s3, s2
	s_bfe_u32 s3, s3, 0x4001b
	s_add_i32 s3, s2, s3
	s_sext_i32_i16 s5, s3
	s_and_b32 s3, s3, 0xfff0
	s_sub_i32 s2, s2, s3
	s_sext_i32_i16 s13, s2
	s_lshl_b32 s2, s5, 2
	s_ashr_i32 s5, s4, 31
	s_andn2_b32 s2, s2, 63
	s_lshl_b32 s6, s13, 6
	s_lshl_b64 s[4:5], s[4:5], 23
	s_add_u32 s7, s14, s4
	s_addc_u32 s16, s15, s5
	s_ashr_i32 s3, s2, 31
	s_lshl_b64 s[18:19], s[2:3], 12
	s_add_u32 s20, s7, s18
	s_addc_u32 s16, s16, s19
	s_ashr_i32 s7, s6, 31
	s_lshl_b64 s[18:19], s[6:7], 2
	s_add_u32 s18, s20, s18
	s_addc_u32 s19, s16, s19
	v_lshl_add_u64 v[0:1], s[18:19], 0, v[96:97]
	v_lshl_add_u64 v[2:3], v[0:1], 0, v[60:61]
	global_load_dwordx4 v[114:117], v[2:3], off nt
	v_lshl_add_u64 v[2:3], v[0:1], 0, v[62:63]
	global_load_dwordx4 v[56:59], v[2:3], off nt
	v_lshl_add_u64 v[2:3], v[0:1], 0, v[64:65]
	global_load_dwordx4 v[52:55], v[2:3], off nt
	v_lshl_add_u64 v[2:3], v[0:1], 0, v[66:67]
	global_load_dwordx4 v[48:51], v[2:3], off nt
	v_lshl_add_u64 v[2:3], v[0:1], 0, v[68:69]
	global_load_dwordx4 v[44:47], v[2:3], off nt
	v_lshl_add_u64 v[2:3], v[0:1], 0, v[70:71]
	global_load_dwordx4 v[40:43], v[2:3], off nt
	v_lshl_add_u64 v[2:3], v[0:1], 0, v[72:73]
	global_load_dwordx4 v[36:39], v[2:3], off nt
	v_lshl_add_u64 v[2:3], v[0:1], 0, v[74:75]
	global_load_dwordx4 v[32:35], v[2:3], off nt
	v_lshl_add_u64 v[2:3], v[0:1], 0, v[76:77]
	global_load_dwordx4 v[28:31], v[2:3], off nt
	v_lshl_add_u64 v[2:3], v[0:1], 0, v[78:79]
	global_load_dwordx4 v[24:27], v[2:3], off nt
	v_lshl_add_u64 v[2:3], v[0:1], 0, v[80:81]
	global_load_dwordx4 v[20:23], v[2:3], off nt
	v_lshl_add_u64 v[2:3], v[0:1], 0, v[82:83]
	global_load_dwordx4 v[16:19], v[2:3], off nt
	v_lshl_add_u64 v[2:3], v[0:1], 0, v[84:85]
	global_load_dwordx4 v[12:15], v[2:3], off nt
	v_lshl_add_u64 v[2:3], v[0:1], 0, v[86:87]
	global_load_dwordx4 v[8:11], v[2:3], off nt
	v_lshl_add_u64 v[2:3], v[0:1], 0, v[88:89]
	global_load_dwordx4 v[4:7], v[2:3], off nt
	v_lshl_add_u64 v[0:1], v[0:1], 0, v[90:91]
	global_load_dwordx4 v[0:3], v[0:1], off nt
	v_add_u32_e32 v111, 0x410, v113
	s_lshl_b32 s7, s13, 7
	s_and_b32 s6, s6, 64
	s_or_b32 s6, s6, s7
	s_bitset1_b32 s6, 7
	s_ashr_i32 s7, s6, 31
	s_add_u32 s13, s21, s4
	s_addc_u32 s16, s22, s5
	s_lshl_b64 s[4:5], s[6:7], 12
	s_add_u32 s4, s13, s4
	s_addc_u32 s5, s16, s5
	s_lshl_b64 s[2:3], s[2:3], 1
	s_add_u32 s2, s4, s2
	s_addc_u32 s3, s5, s3
.Lcvp_1_skip:
	s_waitcnt lgkmcnt(0)
	ds_read2_b32 v[176:177], v112 offset0:65 offset1:73
	ds_read2_b32 v[178:179], v112 offset1:8
	ds_read2_b32 v[180:181], v112 offset0:130 offset1:138
	ds_read2_b32 v[182:183], v112 offset0:195 offset1:203
	v_lshl_add_u64 v[192:193], v[174:175], 0, v[92:93]
	s_waitcnt lgkmcnt(2)
	v_cvt_pk_bf16_f32 v170, v178, v176
	v_add_u32_e32 v176, 0x400, v112
	ds_read2_b32 v[184:185], v176 offset0:4 offset1:12
	ds_read2_b32 v[186:187], v176 offset0:69 offset1:77
	ds_read2_b32 v[188:189], v176 offset0:134 offset1:142
	ds_read2_b32 v[190:191], v176 offset0:199 offset1:207
	s_waitcnt lgkmcnt(4)
	v_cvt_pk_bf16_f32 v171, v180, v182
	v_lshl_add_u64 v[194:195], v[174:175], 0, v[98:99]
	s_waitcnt lgkmcnt(2)
	v_cvt_pk_bf16_f32 v172, v184, v186
	s_waitcnt lgkmcnt(0)
	v_cvt_pk_bf16_f32 v173, v188, v190
	global_store_dwordx4 v[192:193], v[170:173], off
	s_nop 1
	v_cvt_pk_bf16_f32 v170, v179, v177
	v_cvt_pk_bf16_f32 v171, v181, v183
	v_cvt_pk_bf16_f32 v172, v185, v187
	v_cvt_pk_bf16_f32 v173, v189, v191
	v_lshl_add_u64 v[178:179], v[174:175], 0, v[94:95]
	global_store_dwordx4 v[178:179], v[170:173], off
	ds_read2_b32 v[178:179], v112 offset0:81 offset1:89
	ds_read2_b32 v[180:181], v112 offset0:16 offset1:24
	ds_read2_b32 v[182:183], v112 offset0:146 offset1:154
	ds_read2_b32 v[184:185], v112 offset0:211 offset1:219
	ds_read2_b32 v[186:187], v176 offset0:20 offset1:28
	ds_read2_b32 v[188:189], v176 offset0:85 offset1:93
	ds_read2_b32 v[190:191], v176 offset0:150 offset1:158
	ds_read2_b32 v[192:193], v176 offset0:215 offset1:223
	s_waitcnt lgkmcnt(6)
	v_cvt_pk_bf16_f32 v170, v180, v178
	s_waitcnt lgkmcnt(4)
	v_cvt_pk_bf16_f32 v171, v182, v184
	s_waitcnt lgkmcnt(2)
	v_cvt_pk_bf16_f32 v172, v186, v188
	s_waitcnt lgkmcnt(0)
	v_cvt_pk_bf16_f32 v173, v190, v192
	global_store_dwordx4 v[194:195], v[170:173], off
	v_lshl_add_u64 v[194:195], v[174:175], 0, v[102:103]
	s_nop 0
	v_cvt_pk_bf16_f32 v170, v181, v179
	v_cvt_pk_bf16_f32 v171, v183, v185
	v_cvt_pk_bf16_f32 v172, v187, v189
	v_cvt_pk_bf16_f32 v173, v191, v193
	v_lshl_add_u64 v[178:179], v[174:175], 0, v[100:101]
	global_store_dwordx4 v[178:179], v[170:173], off
	ds_read2_b32 v[178:179], v112 offset0:32 offset1:40
	ds_read2_b32 v[180:181], v112 offset0:97 offset1:105
	ds_read2_b32 v[182:183], v112 offset0:162 offset1:170
	ds_read2_b32 v[184:185], v112 offset0:227 offset1:235
	ds_read2_b32 v[186:187], v176 offset0:36 offset1:44
	ds_read2_b32 v[188:189], v176 offset0:101 offset1:109
	ds_read2_b32 v[190:191], v176 offset0:166 offset1:174
	ds_read2_b32 v[192:193], v176 offset0:231 offset1:239
	s_waitcnt lgkmcnt(6)
	v_cvt_pk_bf16_f32 v170, v178, v180
	s_waitcnt lgkmcnt(4)
	v_cvt_pk_bf16_f32 v171, v182, v184
	s_waitcnt lgkmcnt(2)
	v_cvt_pk_bf16_f32 v172, v186, v188
	s_waitcnt lgkmcnt(0)
	v_cvt_pk_bf16_f32 v173, v190, v192
	global_store_dwordx4 v[194:195], v[170:173], off
	s_nop 1
	v_cvt_pk_bf16_f32 v170, v179, v181
	v_cvt_pk_bf16_f32 v171, v183, v185
	v_cvt_pk_bf16_f32 v172, v187, v189
	v_cvt_pk_bf16_f32 v173, v191, v193
	v_lshl_add_u64 v[178:179], v[174:175], 0, v[104:105]
	global_store_dwordx4 v[178:179], v[170:173], off
	ds_read2_b32 v[178:179], v112 offset0:48 offset1:56
	ds_read2_b32 v[180:181], v112 offset0:113 offset1:121
	ds_read2_b32 v[182:183], v112 offset0:178 offset1:186
	ds_read2_b32 v[184:185], v112 offset0:243 offset1:251
	ds_read2_b32 v[186:187], v176 offset0:52 offset1:60
	ds_read2_b32 v[188:189], v176 offset0:117 offset1:125
	ds_read2_b32 v[190:191], v176 offset0:182 offset1:190
	ds_read2_b32 v[176:177], v176 offset0:247 offset1:255
	v_lshl_add_u64 v[192:193], v[174:175], 0, v[106:107]
	s_waitcnt lgkmcnt(6)
	v_cvt_pk_bf16_f32 v170, v178, v180
	s_waitcnt lgkmcnt(4)
	v_cvt_pk_bf16_f32 v171, v182, v184
	s_waitcnt lgkmcnt(2)
	v_cvt_pk_bf16_f32 v172, v186, v188
	s_waitcnt lgkmcnt(0)
	v_cvt_pk_bf16_f32 v173, v190, v176
	global_store_dwordx4 v[192:193], v[170:173], off
	v_lshl_add_u64 v[174:175], v[174:175], 0, v[108:109]
	s_nop 0
	v_cvt_pk_bf16_f32 v170, v179, v181
	v_cvt_pk_bf16_f32 v171, v183, v185
	v_cvt_pk_bf16_f32 v172, v187, v189
	v_cvt_pk_bf16_f32 v173, v191, v177
	global_store_dwordx4 v[174:175], v[170:173], off
	s_waitcnt lgkmcnt(0)
	s_cmpk_lt_i32 s12, 0x1000
	s_cbranch_scc1 .Lcvp_1_loop

.LBB0_1077:
	s_ashr_i32 s4, s16, 31
	s_lshr_b32 s4, s4, 23
	s_add_i32 s4, s16, s4
	s_ashr_i32 s6, s4, 9
	s_and_b32 s4, s4, 0xfe00
	s_sub_i32 s4, s16, s4
	s_sext_i32_i16 s5, s4
	s_bfe_u32 s5, s5, 0x4001b
	s_add_i32 s5, s4, s5
	s_sext_i32_i16 s7, s5
	s_and_b32 s5, s5, 0xfff0
	s_sub_i32 s4, s4, s5
	s_sext_i32_i16 s18, s4
	s_lshl_b32 s4, s7, 2
	s_ashr_i32 s7, s6, 31
	s_andn2_b32 s4, s4, 63
	s_lshl_b32 s12, s18, 6
	s_lshl_b64 s[6:7], s[6:7], 23
	s_waitcnt lgkmcnt(0)
	s_add_u32 s13, s2, s6
	s_addc_u32 s19, s3, s7
	s_ashr_i32 s5, s4, 31
	s_lshl_b64 s[20:21], s[4:5], 12
	s_add_u32 s22, s13, s20
	s_addc_u32 s19, s19, s21
	s_ashr_i32 s13, s12, 31
	s_lshl_b64 s[20:21], s[12:13], 2
	s_add_u32 s20, s22, s20
	s_addc_u32 s21, s19, s21
	v_lshl_add_u64 v[0:1], s[20:21], 0, v[96:97]
	v_lshl_add_u64 v[2:3], v[0:1], 0, v[60:61]
	global_load_dwordx4 v[116:119], v[2:3], off nt
	v_lshl_add_u64 v[2:3], v[0:1], 0, v[62:63]
	global_load_dwordx4 v[56:59], v[2:3], off nt
	v_lshl_add_u64 v[2:3], v[0:1], 0, v[64:65]
	global_load_dwordx4 v[52:55], v[2:3], off nt
	v_lshl_add_u64 v[2:3], v[0:1], 0, v[66:67]
	global_load_dwordx4 v[48:51], v[2:3], off nt
	v_lshl_add_u64 v[2:3], v[0:1], 0, v[68:69]
	global_load_dwordx4 v[44:47], v[2:3], off nt
	v_lshl_add_u64 v[2:3], v[0:1], 0, v[70:71]
	global_load_dwordx4 v[40:43], v[2:3], off nt
	v_lshl_add_u64 v[2:3], v[0:1], 0, v[72:73]
	global_load_dwordx4 v[36:39], v[2:3], off nt
	v_lshl_add_u64 v[2:3], v[0:1], 0, v[74:75]
	global_load_dwordx4 v[32:35], v[2:3], off nt
	v_lshl_add_u64 v[2:3], v[0:1], 0, v[76:77]
	global_load_dwordx4 v[28:31], v[2:3], off nt
	v_lshl_add_u64 v[2:3], v[0:1], 0, v[78:79]
	global_load_dwordx4 v[24:27], v[2:3], off nt
	v_lshl_add_u64 v[2:3], v[0:1], 0, v[80:81]
	global_load_dwordx4 v[20:23], v[2:3], off nt
	v_lshl_add_u64 v[2:3], v[0:1], 0, v[82:83]
	global_load_dwordx4 v[16:19], v[2:3], off nt
	v_lshl_add_u64 v[2:3], v[0:1], 0, v[84:85]
	global_load_dwordx4 v[12:15], v[2:3], off nt
	v_lshl_add_u64 v[2:3], v[0:1], 0, v[86:87]
	global_load_dwordx4 v[8:11], v[2:3], off nt
	v_lshl_add_u64 v[2:3], v[0:1], 0, v[88:89]
	global_load_dwordx4 v[4:7], v[2:3], off nt
	v_lshl_add_u64 v[0:1], v[0:1], 0, v[90:91]
	global_load_dwordx4 v[0:3], v[0:1], off nt
	v_add_u32_e32 v111, 0x410, v114
	s_lshl_b32 s13, s18, 7
	s_and_b32 s13, s13, 0xffffff00
	s_and_b32 s12, s12, 64
	s_or_b32 s12, s13, s12
	s_ashr_i32 s13, s12, 31
	s_add_u32 s18, s23, s6
	s_addc_u32 s19, s24, s7
	s_lshl_b64 s[6:7], s[12:13], 12
	s_add_u32 s6, s18, s6
	s_addc_u32 s7, s19, s7
	s_lshl_b64 s[4:5], s[4:5], 1
	s_add_u32 s4, s6, s4
	s_addc_u32 s5, s7, s5
.Lcvp_2_loop:
	s_waitcnt vmcnt(0) lgkmcnt(0)
	ds_write2_b32 v114, v116, v117 offset1:1
	ds_write2_b32 v114, v118, v119 offset0:2 offset1:3
	ds_write2_b32 v111, v56, v57 offset1:1
	v_add_u32_e32 v56, 0x418, v114
	ds_write2_b32 v56, v58, v59 offset1:1
	v_add_u32_e32 v56, 0x820, v114
	ds_write2_b32 v56, v52, v53 offset1:1
	v_add_u32_e32 v52, 0x828, v114
	ds_write2_b32 v52, v54, v55 offset1:1
	v_add_u32_e32 v52, 0xc30, v114
	ds_write2_b32 v52, v48, v49 offset1:1
	v_add_u32_e32 v48, 0xc38, v114
	ds_write2_b32 v48, v50, v51 offset1:1
	v_add_u32_e32 v48, 0x1040, v114
	ds_write2_b32 v48, v44, v45 offset1:1
	v_add_u32_e32 v44, 0x1048, v114
	ds_write2_b32 v44, v46, v47 offset1:1
	v_add_u32_e32 v44, 0x1450, v114
	ds_write2_b32 v44, v40, v41 offset1:1
	v_add_u32_e32 v40, 0x1458, v114
	ds_write2_b32 v40, v42, v43 offset1:1
	v_add_u32_e32 v40, 0x1860, v114
	ds_write2_b32 v40, v36, v37 offset1:1
	v_add_u32_e32 v36, 0x1868, v114
	ds_write2_b32 v36, v38, v39 offset1:1
	v_add_u32_e32 v36, 0x1c70, v114
	ds_write2_b32 v36, v32, v33 offset1:1
	v_add_u32_e32 v32, 0x1c78, v114
	ds_write2_b32 v32, v34, v35 offset1:1
	v_add_u32_e32 v32, 0x2080, v114
	ds_write2_b32 v32, v28, v29 offset1:1
	v_add_u32_e32 v28, 0x2088, v114
	ds_write2_b32 v28, v30, v31 offset1:1
	v_add_u32_e32 v28, 0x2490, v114
	ds_write2_b32 v28, v24, v25 offset1:1
	v_add_u32_e32 v24, 0x2498, v114
	ds_write2_b32 v24, v26, v27 offset1:1
	v_add_u32_e32 v24, 0x28a0, v114
	ds_write2_b32 v24, v20, v21 offset1:1
	v_add_u32_e32 v20, 0x28a8, v114
	ds_write2_b32 v20, v22, v23 offset1:1
	v_add_u32_e32 v20, 0x2cb0, v114
	ds_write2_b32 v20, v16, v17 offset1:1
	v_add_u32_e32 v16, 0x2cb8, v114
	ds_write2_b32 v16, v18, v19 offset1:1
	v_add_u32_e32 v16, 0x30c0, v114
	ds_write2_b32 v16, v12, v13 offset1:1
	v_add_u32_e32 v12, 0x30c8, v114
	ds_write2_b32 v12, v14, v15 offset1:1
	v_add_u32_e32 v12, 0x34d0, v114
	ds_write2_b32 v12, v8, v9 offset1:1
	v_add_u32_e32 v8, 0x34d8, v114
	ds_write2_b32 v8, v10, v11 offset1:1
	v_add_u32_e32 v8, 0x38e0, v114
	ds_write2_b32 v8, v4, v5 offset1:1
	v_add_u32_e32 v4, 0x38e8, v114
	ds_write2_b32 v4, v6, v7 offset1:1
	v_add_u32_e32 v4, 0x3cf0, v114
	ds_write2_b32 v4, v0, v1 offset1:1
	v_add_u32_e32 v0, 0x3cf8, v114
	ds_write2_b32 v0, v2, v3 offset1:1
	v_mov_b32_e32 v111, v97
	v_lshl_add_u64 v[174:175], s[4:5], 0, v[110:111]
	s_add_i32 s16, s16, s80
	s_cmpk_lt_i32 s16, 0x2000
	s_cbranch_scc0 .Lcvp_2_skip
	s_ashr_i32 s4, s16, 31
	s_lshr_b32 s4, s4, 23
	s_add_i32 s4, s16, s4
	s_ashr_i32 s6, s4, 9
	s_and_b32 s4, s4, 0xfe00
	s_sub_i32 s4, s16, s4
	s_sext_i32_i16 s5, s4
	s_bfe_u32 s5, s5, 0x4001b
	s_add_i32 s5, s4, s5
	s_sext_i32_i16 s7, s5
	s_and_b32 s5, s5, 0xfff0
	s_sub_i32 s4, s4, s5
	s_sext_i32_i16 s18, s4
	s_lshl_b32 s4, s7, 2
	s_ashr_i32 s7, s6, 31
	s_andn2_b32 s4, s4, 63
	s_lshl_b32 s12, s18, 6
	s_lshl_b64 s[6:7], s[6:7], 23
	s_waitcnt lgkmcnt(0)
	s_add_u32 s13, s2, s6
	s_addc_u32 s19, s3, s7
	s_ashr_i32 s5, s4, 31
	s_lshl_b64 s[20:21], s[4:5], 12
	s_add_u32 s22, s13, s20
	s_addc_u32 s19, s19, s21
	s_ashr_i32 s13, s12, 31
	s_lshl_b64 s[20:21], s[12:13], 2
	s_add_u32 s20, s22, s20
	s_addc_u32 s21, s19, s21
	v_lshl_add_u64 v[0:1], s[20:21], 0, v[96:97]
	v_lshl_add_u64 v[2:3], v[0:1], 0, v[60:61]
	global_load_dwordx4 v[116:119], v[2:3], off nt
	v_lshl_add_u64 v[2:3], v[0:1], 0, v[62:63]
	global_load_dwordx4 v[56:59], v[2:3], off nt
	v_lshl_add_u64 v[2:3], v[0:1], 0, v[64:65]
	global_load_dwordx4 v[52:55], v[2:3], off nt
	v_lshl_add_u64 v[2:3], v[0:1], 0, v[66:67]
	global_load_dwordx4 v[48:51], v[2:3], off nt
	v_lshl_add_u64 v[2:3], v[0:1], 0, v[68:69]
	global_load_dwordx4 v[44:47], v[2:3], off nt
	v_lshl_add_u64 v[2:3], v[0:1], 0, v[70:71]
	global_load_dwordx4 v[40:43], v[2:3], off nt
	v_lshl_add_u64 v[2:3], v[0:1], 0, v[72:73]
	global_load_dwordx4 v[36:39], v[2:3], off nt
	v_lshl_add_u64 v[2:3], v[0:1], 0, v[74:75]
	global_load_dwordx4 v[32:35], v[2:3], off nt
	v_lshl_add_u64 v[2:3], v[0:1], 0, v[76:77]
	global_load_dwordx4 v[28:31], v[2:3], off nt
	v_lshl_add_u64 v[2:3], v[0:1], 0, v[78:79]
	global_load_dwordx4 v[24:27], v[2:3], off nt
	v_lshl_add_u64 v[2:3], v[0:1], 0, v[80:81]
	global_load_dwordx4 v[20:23], v[2:3], off nt
	v_lshl_add_u64 v[2:3], v[0:1], 0, v[82:83]
	global_load_dwordx4 v[16:19], v[2:3], off nt
	v_lshl_add_u64 v[2:3], v[0:1], 0, v[84:85]
	global_load_dwordx4 v[12:15], v[2:3], off nt
	v_lshl_add_u64 v[2:3], v[0:1], 0, v[86:87]
	global_load_dwordx4 v[8:11], v[2:3], off nt
	v_lshl_add_u64 v[2:3], v[0:1], 0, v[88:89]
	global_load_dwordx4 v[4:7], v[2:3], off nt
	v_lshl_add_u64 v[0:1], v[0:1], 0, v[90:91]
	global_load_dwordx4 v[0:3], v[0:1], off nt
	v_add_u32_e32 v111, 0x410, v114
	s_lshl_b32 s13, s18, 7
	s_and_b32 s13, s13, 0xffffff00
	s_and_b32 s12, s12, 64
	s_or_b32 s12, s13, s12
	s_ashr_i32 s13, s12, 31
	s_add_u32 s18, s23, s6
	s_addc_u32 s19, s24, s7
	s_lshl_b64 s[6:7], s[12:13], 12
	s_add_u32 s6, s18, s6
	s_addc_u32 s7, s19, s7
	s_lshl_b64 s[4:5], s[4:5], 1
	s_add_u32 s4, s6, s4
	s_addc_u32 s5, s7, s5
.Lcvp_2_skip:
	s_waitcnt lgkmcnt(0)
	ds_read2_b32 v[176:177], v113 offset0:65 offset1:73
	ds_read2_b32 v[178:179], v113 offset1:8
	ds_read2_b32 v[180:181], v113 offset0:130 offset1:138
	ds_read2_b32 v[182:183], v113 offset0:195 offset1:203
	v_lshl_add_u64 v[192:193], v[174:175], 0, v[92:93]
	s_waitcnt lgkmcnt(2)
	v_cvt_pk_bf16_f32 v170, v178, v176
	v_add_u32_e32 v176, 0x400, v113
	ds_read2_b32 v[184:185], v176 offset0:4 offset1:12
	ds_read2_b32 v[186:187], v176 offset0:69 offset1:77
	ds_read2_b32 v[188:189], v176 offset0:134 offset1:142
	ds_read2_b32 v[190:191], v176 offset0:199 offset1:207
	s_waitcnt lgkmcnt(4)
	v_cvt_pk_bf16_f32 v171, v180, v182
	v_lshl_add_u64 v[194:195], v[174:175], 0, v[98:99]
	s_waitcnt lgkmcnt(2)
	v_cvt_pk_bf16_f32 v172, v184, v186
	s_waitcnt lgkmcnt(0)
	v_cvt_pk_bf16_f32 v173, v188, v190
	global_store_dwordx4 v[192:193], v[170:173], off
	s_nop 1
	v_cvt_pk_bf16_f32 v170, v179, v177
	v_cvt_pk_bf16_f32 v171, v181, v183
	v_cvt_pk_bf16_f32 v172, v185, v187
	v_cvt_pk_bf16_f32 v173, v189, v191
	v_lshl_add_u64 v[178:179], v[174:175], 0, v[94:95]
	global_store_dwordx4 v[178:179], v[170:173], off
	ds_read2_b32 v[178:179], v113 offset0:81 offset1:89
	ds_read2_b32 v[180:181], v113 offset0:16 offset1:24
	ds_read2_b32 v[182:183], v113 offset0:146 offset1:154
	ds_read2_b32 v[184:185], v113 offset0:211 offset1:219
	ds_read2_b32 v[186:187], v176 offset0:20 offset1:28
	ds_read2_b32 v[188:189], v176 offset0:85 offset1:93
	ds_read2_b32 v[190:191], v176 offset0:150 offset1:158
	ds_read2_b32 v[192:193], v176 offset0:215 offset1:223
	s_waitcnt lgkmcnt(6)
	v_cvt_pk_bf16_f32 v170, v180, v178
	s_waitcnt lgkmcnt(4)
	v_cvt_pk_bf16_f32 v171, v182, v184
	s_waitcnt lgkmcnt(2)
	v_cvt_pk_bf16_f32 v172, v186, v188
	s_waitcnt lgkmcnt(0)
	v_cvt_pk_bf16_f32 v173, v190, v192
	global_store_dwordx4 v[194:195], v[170:173], off
	v_lshl_add_u64 v[194:195], v[174:175], 0, v[102:103]
	s_nop 0
	v_cvt_pk_bf16_f32 v170, v181, v179
	v_cvt_pk_bf16_f32 v171, v183, v185
	v_cvt_pk_bf16_f32 v172, v187, v189
	v_cvt_pk_bf16_f32 v173, v191, v193
	v_lshl_add_u64 v[178:179], v[174:175], 0, v[100:101]
	global_store_dwordx4 v[178:179], v[170:173], off
	ds_read2_b32 v[178:179], v113 offset0:32 offset1:40
	ds_read2_b32 v[180:181], v113 offset0:97 offset1:105
	ds_read2_b32 v[182:183], v113 offset0:162 offset1:170
	ds_read2_b32 v[184:185], v113 offset0:227 offset1:235
	ds_read2_b32 v[186:187], v176 offset0:36 offset1:44
	ds_read2_b32 v[188:189], v176 offset0:101 offset1:109
	ds_read2_b32 v[190:191], v176 offset0:166 offset1:174
	ds_read2_b32 v[192:193], v176 offset0:231 offset1:239
	s_waitcnt lgkmcnt(6)
	v_cvt_pk_bf16_f32 v170, v178, v180
	s_waitcnt lgkmcnt(4)
	v_cvt_pk_bf16_f32 v171, v182, v184
	s_waitcnt lgkmcnt(2)
	v_cvt_pk_bf16_f32 v172, v186, v188
	s_waitcnt lgkmcnt(0)
	v_cvt_pk_bf16_f32 v173, v190, v192
	global_store_dwordx4 v[194:195], v[170:173], off
	s_nop 1
	v_cvt_pk_bf16_f32 v170, v179, v181
	v_cvt_pk_bf16_f32 v171, v183, v185
	v_cvt_pk_bf16_f32 v172, v187, v189
	v_cvt_pk_bf16_f32 v173, v191, v193
	v_lshl_add_u64 v[178:179], v[174:175], 0, v[104:105]
	global_store_dwordx4 v[178:179], v[170:173], off
	ds_read2_b32 v[178:179], v113 offset0:48 offset1:56
	ds_read2_b32 v[180:181], v113 offset0:113 offset1:121
	ds_read2_b32 v[182:183], v113 offset0:178 offset1:186
	ds_read2_b32 v[184:185], v113 offset0:243 offset1:251
	ds_read2_b32 v[186:187], v176 offset0:52 offset1:60
	ds_read2_b32 v[188:189], v176 offset0:117 offset1:125
	ds_read2_b32 v[190:191], v176 offset0:182 offset1:190
	ds_read2_b32 v[176:177], v176 offset0:247 offset1:255
	v_lshl_add_u64 v[192:193], v[174:175], 0, v[106:107]
	s_waitcnt lgkmcnt(6)
	v_cvt_pk_bf16_f32 v170, v178, v180
	s_waitcnt lgkmcnt(4)
	v_cvt_pk_bf16_f32 v171, v182, v184
	s_waitcnt lgkmcnt(2)
	v_cvt_pk_bf16_f32 v172, v186, v188
	s_waitcnt lgkmcnt(0)
	v_cvt_pk_bf16_f32 v173, v190, v176
	global_store_dwordx4 v[192:193], v[170:173], off
	v_lshl_add_u64 v[174:175], v[174:175], 0, v[108:109]
	s_nop 0
	v_cvt_pk_bf16_f32 v170, v179, v181
	v_cvt_pk_bf16_f32 v171, v183, v185
	v_cvt_pk_bf16_f32 v172, v187, v189
	v_cvt_pk_bf16_f32 v173, v191, v177
	global_store_dwordx4 v[174:175], v[170:173], off
	s_waitcnt lgkmcnt(0)
	s_cmpk_lt_i32 s16, 0x2000
	s_cbranch_scc1 .Lcvp_2_loop

.LBB0_1080:
	s_ashr_i32 s4, s14, 31
	s_lshr_b32 s4, s4, 23
	s_add_i32 s4, s14, s4
	s_ashr_i32 s6, s4, 9
	s_and_b32 s4, s4, 0xfe00
	s_sub_i32 s4, s14, s4
	s_sext_i32_i16 s5, s4
	s_bfe_u32 s5, s5, 0x4001b
	s_add_i32 s5, s4, s5
	s_sext_i32_i16 s7, s5
	s_and_b32 s5, s5, 0xfff0
	s_sub_i32 s4, s4, s5
	s_sext_i32_i16 s15, s4
	s_lshl_b32 s4, s7, 2
	s_ashr_i32 s7, s6, 31
	s_andn2_b32 s4, s4, 63
	s_lshl_b32 s12, s15, 6
	s_lshl_b64 s[6:7], s[6:7], 23
	s_waitcnt lgkmcnt(0)
	s_add_u32 s13, s2, s6
	s_addc_u32 s16, s3, s7
	s_ashr_i32 s5, s4, 31
	s_lshl_b64 s[18:19], s[4:5], 12
	s_add_u32 s20, s13, s18
	s_addc_u32 s16, s16, s19
	s_ashr_i32 s13, s12, 31
	s_lshl_b64 s[18:19], s[12:13], 2
	s_add_u32 s18, s20, s18
	s_addc_u32 s19, s16, s19
	v_lshl_add_u64 v[0:1], s[18:19], 0, v[96:97]
	v_lshl_add_u64 v[2:3], v[0:1], 0, v[60:61]
	global_load_dwordx4 v[114:117], v[2:3], off nt
	v_lshl_add_u64 v[2:3], v[0:1], 0, v[62:63]
	global_load_dwordx4 v[56:59], v[2:3], off nt
	v_lshl_add_u64 v[2:3], v[0:1], 0, v[64:65]
	global_load_dwordx4 v[52:55], v[2:3], off nt
	v_lshl_add_u64 v[2:3], v[0:1], 0, v[66:67]
	global_load_dwordx4 v[48:51], v[2:3], off nt
	v_lshl_add_u64 v[2:3], v[0:1], 0, v[68:69]
	global_load_dwordx4 v[44:47], v[2:3], off nt
	v_lshl_add_u64 v[2:3], v[0:1], 0, v[70:71]
	global_load_dwordx4 v[40:43], v[2:3], off nt
	v_lshl_add_u64 v[2:3], v[0:1], 0, v[72:73]
	global_load_dwordx4 v[36:39], v[2:3], off nt
	v_lshl_add_u64 v[2:3], v[0:1], 0, v[74:75]
	global_load_dwordx4 v[32:35], v[2:3], off nt
	v_lshl_add_u64 v[2:3], v[0:1], 0, v[76:77]
	global_load_dwordx4 v[28:31], v[2:3], off nt
	v_lshl_add_u64 v[2:3], v[0:1], 0, v[78:79]
	global_load_dwordx4 v[24:27], v[2:3], off nt
	v_lshl_add_u64 v[2:3], v[0:1], 0, v[80:81]
	global_load_dwordx4 v[20:23], v[2:3], off nt
	v_lshl_add_u64 v[2:3], v[0:1], 0, v[82:83]
	global_load_dwordx4 v[16:19], v[2:3], off nt
	v_lshl_add_u64 v[2:3], v[0:1], 0, v[84:85]
	global_load_dwordx4 v[12:15], v[2:3], off nt
	v_lshl_add_u64 v[2:3], v[0:1], 0, v[86:87]
	global_load_dwordx4 v[8:11], v[2:3], off nt
	v_lshl_add_u64 v[2:3], v[0:1], 0, v[88:89]
	global_load_dwordx4 v[4:7], v[2:3], off nt
	v_lshl_add_u64 v[0:1], v[0:1], 0, v[90:91]
	global_load_dwordx4 v[0:3], v[0:1], off nt
	v_add_u32_e32 v111, 0x410, v113
	s_lshl_b32 s13, s15, 7
	s_and_b32 s12, s12, 64
	s_or_b32 s12, s12, s13
	s_bitset1_b32 s12, 7
	s_ashr_i32 s13, s12, 31
	s_add_u32 s15, s23, s6
	s_addc_u32 s16, s24, s7
	s_lshl_b64 s[6:7], s[12:13], 12
	s_add_u32 s6, s15, s6
	s_addc_u32 s7, s16, s7
	s_lshl_b64 s[4:5], s[4:5], 1
	s_add_u32 s4, s6, s4
	s_addc_u32 s5, s7, s5
.Lcvp_3_loop:
	s_waitcnt vmcnt(0) lgkmcnt(0)
	ds_write2_b32 v113, v114, v115 offset1:1
	ds_write2_b32 v113, v116, v117 offset0:2 offset1:3
	ds_write2_b32 v111, v56, v57 offset1:1
	v_add_u32_e32 v56, 0x418, v113
	ds_write2_b32 v56, v58, v59 offset1:1
	v_add_u32_e32 v56, 0x820, v113
	ds_write2_b32 v56, v52, v53 offset1:1
	v_add_u32_e32 v52, 0x828, v113
	ds_write2_b32 v52, v54, v55 offset1:1
	v_add_u32_e32 v52, 0xc30, v113
	ds_write2_b32 v52, v48, v49 offset1:1
	v_add_u32_e32 v48, 0xc38, v113
	ds_write2_b32 v48, v50, v51 offset1:1
	v_add_u32_e32 v48, 0x1040, v113
	ds_write2_b32 v48, v44, v45 offset1:1
	v_add_u32_e32 v44, 0x1048, v113
	ds_write2_b32 v44, v46, v47 offset1:1
	v_add_u32_e32 v44, 0x1450, v113
	ds_write2_b32 v44, v40, v41 offset1:1
	v_add_u32_e32 v40, 0x1458, v113
	ds_write2_b32 v40, v42, v43 offset1:1
	v_add_u32_e32 v40, 0x1860, v113
	ds_write2_b32 v40, v36, v37 offset1:1
	v_add_u32_e32 v36, 0x1868, v113
	ds_write2_b32 v36, v38, v39 offset1:1
	v_add_u32_e32 v36, 0x1c70, v113
	ds_write2_b32 v36, v32, v33 offset1:1
	v_add_u32_e32 v32, 0x1c78, v113
	ds_write2_b32 v32, v34, v35 offset1:1
	v_add_u32_e32 v32, 0x2080, v113
	ds_write2_b32 v32, v28, v29 offset1:1
	v_add_u32_e32 v28, 0x2088, v113
	ds_write2_b32 v28, v30, v31 offset1:1
	v_add_u32_e32 v28, 0x2490, v113
	ds_write2_b32 v28, v24, v25 offset1:1
	v_add_u32_e32 v24, 0x2498, v113
	ds_write2_b32 v24, v26, v27 offset1:1
	v_add_u32_e32 v24, 0x28a0, v113
	ds_write2_b32 v24, v20, v21 offset1:1
	v_add_u32_e32 v20, 0x28a8, v113
	ds_write2_b32 v20, v22, v23 offset1:1
	v_add_u32_e32 v20, 0x2cb0, v113
	ds_write2_b32 v20, v16, v17 offset1:1
	v_add_u32_e32 v16, 0x2cb8, v113
	ds_write2_b32 v16, v18, v19 offset1:1
	v_add_u32_e32 v16, 0x30c0, v113
	ds_write2_b32 v16, v12, v13 offset1:1
	v_add_u32_e32 v12, 0x30c8, v113
	ds_write2_b32 v12, v14, v15 offset1:1
	v_add_u32_e32 v12, 0x34d0, v113
	ds_write2_b32 v12, v8, v9 offset1:1
	v_add_u32_e32 v8, 0x34d8, v113
	ds_write2_b32 v8, v10, v11 offset1:1
	v_add_u32_e32 v8, 0x38e0, v113
	ds_write2_b32 v8, v4, v5 offset1:1
	v_add_u32_e32 v4, 0x38e8, v113
	ds_write2_b32 v4, v6, v7 offset1:1
	v_add_u32_e32 v4, 0x3cf0, v113
	ds_write2_b32 v4, v0, v1 offset1:1
	v_add_u32_e32 v0, 0x3cf8, v113
	ds_write2_b32 v0, v2, v3 offset1:1
	v_mov_b32_e32 v111, v97
	v_lshl_add_u64 v[174:175], s[4:5], 0, v[110:111]
	s_add_i32 s14, s14, s80
	s_cmpk_lt_i32 s14, 0x1000
	s_cbranch_scc0 .Lcvp_3_skip
	s_ashr_i32 s4, s14, 31
	s_lshr_b32 s4, s4, 23
	s_add_i32 s4, s14, s4
	s_ashr_i32 s6, s4, 9
	s_and_b32 s4, s4, 0xfe00
	s_sub_i32 s4, s14, s4
	s_sext_i32_i16 s5, s4
	s_bfe_u32 s5, s5, 0x4001b
	s_add_i32 s5, s4, s5
	s_sext_i32_i16 s7, s5
	s_and_b32 s5, s5, 0xfff0
	s_sub_i32 s4, s4, s5
	s_sext_i32_i16 s15, s4
	s_lshl_b32 s4, s7, 2
	s_ashr_i32 s7, s6, 31
	s_andn2_b32 s4, s4, 63
	s_lshl_b32 s12, s15, 6
	s_lshl_b64 s[6:7], s[6:7], 23
	s_waitcnt lgkmcnt(0)
	s_add_u32 s13, s2, s6
	s_addc_u32 s16, s3, s7
	s_ashr_i32 s5, s4, 31
	s_lshl_b64 s[18:19], s[4:5], 12
	s_add_u32 s20, s13, s18
	s_addc_u32 s16, s16, s19
	s_ashr_i32 s13, s12, 31
	s_lshl_b64 s[18:19], s[12:13], 2
	s_add_u32 s18, s20, s18
	s_addc_u32 s19, s16, s19
	v_lshl_add_u64 v[0:1], s[18:19], 0, v[96:97]
	v_lshl_add_u64 v[2:3], v[0:1], 0, v[60:61]
	global_load_dwordx4 v[114:117], v[2:3], off nt
	v_lshl_add_u64 v[2:3], v[0:1], 0, v[62:63]
	global_load_dwordx4 v[56:59], v[2:3], off nt
	v_lshl_add_u64 v[2:3], v[0:1], 0, v[64:65]
	global_load_dwordx4 v[52:55], v[2:3], off nt
	v_lshl_add_u64 v[2:3], v[0:1], 0, v[66:67]
	global_load_dwordx4 v[48:51], v[2:3], off nt
	v_lshl_add_u64 v[2:3], v[0:1], 0, v[68:69]
	global_load_dwordx4 v[44:47], v[2:3], off nt
	v_lshl_add_u64 v[2:3], v[0:1], 0, v[70:71]
	global_load_dwordx4 v[40:43], v[2:3], off nt
	v_lshl_add_u64 v[2:3], v[0:1], 0, v[72:73]
	global_load_dwordx4 v[36:39], v[2:3], off nt
	v_lshl_add_u64 v[2:3], v[0:1], 0, v[74:75]
	global_load_dwordx4 v[32:35], v[2:3], off nt
	v_lshl_add_u64 v[2:3], v[0:1], 0, v[76:77]
	global_load_dwordx4 v[28:31], v[2:3], off nt
	v_lshl_add_u64 v[2:3], v[0:1], 0, v[78:79]
	global_load_dwordx4 v[24:27], v[2:3], off nt
	v_lshl_add_u64 v[2:3], v[0:1], 0, v[80:81]
	global_load_dwordx4 v[20:23], v[2:3], off nt
	v_lshl_add_u64 v[2:3], v[0:1], 0, v[82:83]
	global_load_dwordx4 v[16:19], v[2:3], off nt
	v_lshl_add_u64 v[2:3], v[0:1], 0, v[84:85]
	global_load_dwordx4 v[12:15], v[2:3], off nt
	v_lshl_add_u64 v[2:3], v[0:1], 0, v[86:87]
	global_load_dwordx4 v[8:11], v[2:3], off nt
	v_lshl_add_u64 v[2:3], v[0:1], 0, v[88:89]
	global_load_dwordx4 v[4:7], v[2:3], off nt
	v_lshl_add_u64 v[0:1], v[0:1], 0, v[90:91]
	global_load_dwordx4 v[0:3], v[0:1], off nt
	v_add_u32_e32 v111, 0x410, v113
	s_lshl_b32 s13, s15, 7
	s_and_b32 s12, s12, 64
	s_or_b32 s12, s12, s13
	s_bitset1_b32 s12, 7
	s_ashr_i32 s13, s12, 31
	s_add_u32 s15, s23, s6
	s_addc_u32 s16, s24, s7
	s_lshl_b64 s[6:7], s[12:13], 12
	s_add_u32 s6, s15, s6
	s_addc_u32 s7, s16, s7
	s_lshl_b64 s[4:5], s[4:5], 1
	s_add_u32 s4, s6, s4
	s_addc_u32 s5, s7, s5
.Lcvp_3_skip:
	s_waitcnt lgkmcnt(0)
	ds_read2_b32 v[176:177], v112 offset0:65 offset1:73
	ds_read2_b32 v[178:179], v112 offset1:8
	ds_read2_b32 v[180:181], v112 offset0:130 offset1:138
	ds_read2_b32 v[182:183], v112 offset0:195 offset1:203
	v_lshl_add_u64 v[192:193], v[174:175], 0, v[92:93]
	s_waitcnt lgkmcnt(2)
	v_cvt_pk_bf16_f32 v170, v178, v176
	v_add_u32_e32 v176, 0x400, v112
	ds_read2_b32 v[184:185], v176 offset0:4 offset1:12
	ds_read2_b32 v[186:187], v176 offset0:69 offset1:77
	ds_read2_b32 v[188:189], v176 offset0:134 offset1:142
	ds_read2_b32 v[190:191], v176 offset0:199 offset1:207
	s_waitcnt lgkmcnt(4)
	v_cvt_pk_bf16_f32 v171, v180, v182
	v_lshl_add_u64 v[194:195], v[174:175], 0, v[98:99]
	s_waitcnt lgkmcnt(2)
	v_cvt_pk_bf16_f32 v172, v184, v186
	s_waitcnt lgkmcnt(0)
	v_cvt_pk_bf16_f32 v173, v188, v190
	global_store_dwordx4 v[192:193], v[170:173], off
	s_nop 1
	v_cvt_pk_bf16_f32 v170, v179, v177
	v_cvt_pk_bf16_f32 v171, v181, v183
	v_cvt_pk_bf16_f32 v172, v185, v187
	v_cvt_pk_bf16_f32 v173, v189, v191
	v_lshl_add_u64 v[178:179], v[174:175], 0, v[94:95]
	global_store_dwordx4 v[178:179], v[170:173], off
	ds_read2_b32 v[178:179], v112 offset0:81 offset1:89
	ds_read2_b32 v[180:181], v112 offset0:16 offset1:24
	ds_read2_b32 v[182:183], v112 offset0:146 offset1:154
	ds_read2_b32 v[184:185], v112 offset0:211 offset1:219
	ds_read2_b32 v[186:187], v176 offset0:20 offset1:28
	ds_read2_b32 v[188:189], v176 offset0:85 offset1:93
	ds_read2_b32 v[190:191], v176 offset0:150 offset1:158
	ds_read2_b32 v[192:193], v176 offset0:215 offset1:223
	s_waitcnt lgkmcnt(6)
	v_cvt_pk_bf16_f32 v170, v180, v178
	s_waitcnt lgkmcnt(4)
	v_cvt_pk_bf16_f32 v171, v182, v184
	s_waitcnt lgkmcnt(2)
	v_cvt_pk_bf16_f32 v172, v186, v188
	s_waitcnt lgkmcnt(0)
	v_cvt_pk_bf16_f32 v173, v190, v192
	global_store_dwordx4 v[194:195], v[170:173], off
	v_lshl_add_u64 v[194:195], v[174:175], 0, v[102:103]
	s_nop 0
	v_cvt_pk_bf16_f32 v170, v181, v179
	v_cvt_pk_bf16_f32 v171, v183, v185
	v_cvt_pk_bf16_f32 v172, v187, v189
	v_cvt_pk_bf16_f32 v173, v191, v193
	v_lshl_add_u64 v[178:179], v[174:175], 0, v[100:101]
	global_store_dwordx4 v[178:179], v[170:173], off
	ds_read2_b32 v[178:179], v112 offset0:32 offset1:40
	ds_read2_b32 v[180:181], v112 offset0:97 offset1:105
	ds_read2_b32 v[182:183], v112 offset0:162 offset1:170
	ds_read2_b32 v[184:185], v112 offset0:227 offset1:235
	ds_read2_b32 v[186:187], v176 offset0:36 offset1:44
	ds_read2_b32 v[188:189], v176 offset0:101 offset1:109
	ds_read2_b32 v[190:191], v176 offset0:166 offset1:174
	ds_read2_b32 v[192:193], v176 offset0:231 offset1:239
	s_waitcnt lgkmcnt(6)
	v_cvt_pk_bf16_f32 v170, v178, v180
	s_waitcnt lgkmcnt(4)
	v_cvt_pk_bf16_f32 v171, v182, v184
	s_waitcnt lgkmcnt(2)
	v_cvt_pk_bf16_f32 v172, v186, v188
	s_waitcnt lgkmcnt(0)
	v_cvt_pk_bf16_f32 v173, v190, v192
	global_store_dwordx4 v[194:195], v[170:173], off
	s_nop 1
	v_cvt_pk_bf16_f32 v170, v179, v181
	v_cvt_pk_bf16_f32 v171, v183, v185
	v_cvt_pk_bf16_f32 v172, v187, v189
	v_cvt_pk_bf16_f32 v173, v191, v193
	v_lshl_add_u64 v[178:179], v[174:175], 0, v[104:105]
	global_store_dwordx4 v[178:179], v[170:173], off
	ds_read2_b32 v[178:179], v112 offset0:48 offset1:56
	ds_read2_b32 v[180:181], v112 offset0:113 offset1:121
	ds_read2_b32 v[182:183], v112 offset0:178 offset1:186
	ds_read2_b32 v[184:185], v112 offset0:243 offset1:251
	ds_read2_b32 v[186:187], v176 offset0:52 offset1:60
	ds_read2_b32 v[188:189], v176 offset0:117 offset1:125
	ds_read2_b32 v[190:191], v176 offset0:182 offset1:190
	ds_read2_b32 v[176:177], v176 offset0:247 offset1:255
	v_lshl_add_u64 v[192:193], v[174:175], 0, v[106:107]
	s_waitcnt lgkmcnt(6)
	v_cvt_pk_bf16_f32 v170, v178, v180
	s_waitcnt lgkmcnt(4)
	v_cvt_pk_bf16_f32 v171, v182, v184
	s_waitcnt lgkmcnt(2)
	v_cvt_pk_bf16_f32 v172, v186, v188
	s_waitcnt lgkmcnt(0)
	v_cvt_pk_bf16_f32 v173, v190, v176
	global_store_dwordx4 v[192:193], v[170:173], off
	v_lshl_add_u64 v[174:175], v[174:175], 0, v[108:109]
	s_nop 0
	v_cvt_pk_bf16_f32 v170, v179, v181
	v_cvt_pk_bf16_f32 v171, v183, v185
	v_cvt_pk_bf16_f32 v172, v187, v189
	v_cvt_pk_bf16_f32 v173, v191, v177
	global_store_dwordx4 v[174:175], v[170:173], off
	s_waitcnt lgkmcnt(0)
	s_cmpk_lt_i32 s14, 0x1000
	s_cbranch_scc1 .Lcvp_3_loop

.LBB0_1164:
	s_ashr_i32 s2, s9, 31
	s_lshr_b32 s2, s2, 23
	s_add_i32 s2, s9, s2
	s_ashr_i32 s4, s2, 9
	s_and_b32 s2, s2, 0xfe00
	s_sub_i32 s2, s9, s2
	s_sext_i32_i16 s3, s2
	s_bfe_u32 s3, s3, 0x4001b
	s_add_i32 s3, s2, s3
	s_sext_i32_i16 s5, s3
	s_and_b32 s3, s3, 0xfff0
	s_sub_i32 s2, s2, s3
	s_sext_i32_i16 s13, s2
	s_lshl_b32 s2, s5, 2
	s_ashr_i32 s5, s4, 31
	s_andn2_b32 s2, s2, 63
	s_lshl_b32 s6, s13, 6
	s_lshl_b64 s[4:5], s[4:5], 23
	s_add_u32 s7, s11, s4
	s_addc_u32 s16, s12, s5
	s_ashr_i32 s3, s2, 31
	s_lshl_b64 s[14:15], s[2:3], 12
	s_add_u32 s18, s7, s14
	s_addc_u32 s16, s16, s15
	s_ashr_i32 s7, s6, 31
	s_lshl_b64 s[14:15], s[6:7], 2
	s_add_u32 s14, s18, s14
	s_addc_u32 s15, s16, s15
	v_lshl_add_u64 v[0:1], s[14:15], 0, v[96:97]
	v_lshl_add_u64 v[2:3], v[0:1], 0, v[60:61]
	global_load_dwordx4 v[116:119], v[2:3], off nt
	v_lshl_add_u64 v[2:3], v[0:1], 0, v[62:63]
	global_load_dwordx4 v[56:59], v[2:3], off nt
	v_lshl_add_u64 v[2:3], v[0:1], 0, v[64:65]
	global_load_dwordx4 v[52:55], v[2:3], off nt
	v_lshl_add_u64 v[2:3], v[0:1], 0, v[66:67]
	global_load_dwordx4 v[48:51], v[2:3], off nt
	v_lshl_add_u64 v[2:3], v[0:1], 0, v[68:69]
	global_load_dwordx4 v[44:47], v[2:3], off nt
	v_lshl_add_u64 v[2:3], v[0:1], 0, v[70:71]
	global_load_dwordx4 v[40:43], v[2:3], off nt
	v_lshl_add_u64 v[2:3], v[0:1], 0, v[72:73]
	global_load_dwordx4 v[36:39], v[2:3], off nt
	v_lshl_add_u64 v[2:3], v[0:1], 0, v[74:75]
	global_load_dwordx4 v[32:35], v[2:3], off nt
	v_lshl_add_u64 v[2:3], v[0:1], 0, v[76:77]
	global_load_dwordx4 v[28:31], v[2:3], off nt
	v_lshl_add_u64 v[2:3], v[0:1], 0, v[78:79]
	global_load_dwordx4 v[24:27], v[2:3], off nt
	v_lshl_add_u64 v[2:3], v[0:1], 0, v[80:81]
	global_load_dwordx4 v[20:23], v[2:3], off nt
	v_lshl_add_u64 v[2:3], v[0:1], 0, v[82:83]
	global_load_dwordx4 v[16:19], v[2:3], off nt
	v_lshl_add_u64 v[2:3], v[0:1], 0, v[84:85]
	global_load_dwordx4 v[12:15], v[2:3], off nt
	v_lshl_add_u64 v[2:3], v[0:1], 0, v[86:87]
	global_load_dwordx4 v[8:11], v[2:3], off nt
	v_lshl_add_u64 v[2:3], v[0:1], 0, v[88:89]
	global_load_dwordx4 v[4:7], v[2:3], off nt
	v_lshl_add_u64 v[0:1], v[0:1], 0, v[90:91]
	global_load_dwordx4 v[0:3], v[0:1], off nt
	v_add_u32_e32 v111, 0x410, v114
	s_lshl_b32 s7, s13, 7
	s_and_b32 s6, s6, 64
	s_or_b32 s6, s6, s7
	s_bitset1_b32 s6, 7
	s_ashr_i32 s7, s6, 31
	s_add_u32 s13, s21, s4
	s_addc_u32 s14, s22, s5
	s_lshl_b64 s[4:5], s[6:7], 12
	s_add_u32 s4, s13, s4
	s_addc_u32 s5, s14, s5
	s_lshl_b64 s[2:3], s[2:3], 1
	s_add_u32 s2, s4, s2
	s_addc_u32 s3, s5, s3
.Lcvp_4_loop:
	s_waitcnt vmcnt(0) lgkmcnt(0)
	ds_write2_b32 v114, v116, v117 offset1:1
	ds_write2_b32 v114, v118, v119 offset0:2 offset1:3
	ds_write2_b32 v111, v56, v57 offset1:1
	v_add_u32_e32 v56, 0x418, v114
	ds_write2_b32 v56, v58, v59 offset1:1
	v_add_u32_e32 v56, 0x820, v114
	ds_write2_b32 v56, v52, v53 offset1:1
	v_add_u32_e32 v52, 0x828, v114
	ds_write2_b32 v52, v54, v55 offset1:1
	v_add_u32_e32 v52, 0xc30, v114
	ds_write2_b32 v52, v48, v49 offset1:1
	v_add_u32_e32 v48, 0xc38, v114
	ds_write2_b32 v48, v50, v51 offset1:1
	v_add_u32_e32 v48, 0x1040, v114
	ds_write2_b32 v48, v44, v45 offset1:1
	v_add_u32_e32 v44, 0x1048, v114
	ds_write2_b32 v44, v46, v47 offset1:1
	v_add_u32_e32 v44, 0x1450, v114
	ds_write2_b32 v44, v40, v41 offset1:1
	v_add_u32_e32 v40, 0x1458, v114
	ds_write2_b32 v40, v42, v43 offset1:1
	v_add_u32_e32 v40, 0x1860, v114
	ds_write2_b32 v40, v36, v37 offset1:1
	v_add_u32_e32 v36, 0x1868, v114
	ds_write2_b32 v36, v38, v39 offset1:1
	v_add_u32_e32 v36, 0x1c70, v114
	ds_write2_b32 v36, v32, v33 offset1:1
	v_add_u32_e32 v32, 0x1c78, v114
	ds_write2_b32 v32, v34, v35 offset1:1
	v_add_u32_e32 v32, 0x2080, v114
	ds_write2_b32 v32, v28, v29 offset1:1
	v_add_u32_e32 v28, 0x2088, v114
	ds_write2_b32 v28, v30, v31 offset1:1
	v_add_u32_e32 v28, 0x2490, v114
	ds_write2_b32 v28, v24, v25 offset1:1
	v_add_u32_e32 v24, 0x2498, v114
	ds_write2_b32 v24, v26, v27 offset1:1
	v_add_u32_e32 v24, 0x28a0, v114
	ds_write2_b32 v24, v20, v21 offset1:1
	v_add_u32_e32 v20, 0x28a8, v114
	ds_write2_b32 v20, v22, v23 offset1:1
	v_add_u32_e32 v20, 0x2cb0, v114
	ds_write2_b32 v20, v16, v17 offset1:1
	v_add_u32_e32 v16, 0x2cb8, v114
	ds_write2_b32 v16, v18, v19 offset1:1
	v_add_u32_e32 v16, 0x30c0, v114
	ds_write2_b32 v16, v12, v13 offset1:1
	v_add_u32_e32 v12, 0x30c8, v114
	ds_write2_b32 v12, v14, v15 offset1:1
	v_add_u32_e32 v12, 0x34d0, v114
	ds_write2_b32 v12, v8, v9 offset1:1
	v_add_u32_e32 v8, 0x34d8, v114
	ds_write2_b32 v8, v10, v11 offset1:1
	v_add_u32_e32 v8, 0x38e0, v114
	ds_write2_b32 v8, v4, v5 offset1:1
	v_add_u32_e32 v4, 0x38e8, v114
	ds_write2_b32 v4, v6, v7 offset1:1
	v_add_u32_e32 v4, 0x3cf0, v114
	ds_write2_b32 v4, v0, v1 offset1:1
	v_add_u32_e32 v0, 0x3cf8, v114
	ds_write2_b32 v0, v2, v3 offset1:1
	v_mov_b32_e32 v111, v97
	v_lshl_add_u64 v[174:175], s[2:3], 0, v[110:111]
	s_add_i32 s9, s9, s80
	s_cmpk_lt_i32 s9, 0x1000
	s_cbranch_scc0 .Lcvp_4_skip
	s_ashr_i32 s2, s9, 31
	s_lshr_b32 s2, s2, 23
	s_add_i32 s2, s9, s2
	s_ashr_i32 s4, s2, 9
	s_and_b32 s2, s2, 0xfe00
	s_sub_i32 s2, s9, s2
	s_sext_i32_i16 s3, s2
	s_bfe_u32 s3, s3, 0x4001b
	s_add_i32 s3, s2, s3
	s_sext_i32_i16 s5, s3
	s_and_b32 s3, s3, 0xfff0
	s_sub_i32 s2, s2, s3
	s_sext_i32_i16 s13, s2
	s_lshl_b32 s2, s5, 2
	s_ashr_i32 s5, s4, 31
	s_andn2_b32 s2, s2, 63
	s_lshl_b32 s6, s13, 6
	s_lshl_b64 s[4:5], s[4:5], 23
	s_add_u32 s7, s11, s4
	s_addc_u32 s16, s12, s5
	s_ashr_i32 s3, s2, 31
	s_lshl_b64 s[14:15], s[2:3], 12
	s_add_u32 s18, s7, s14
	s_addc_u32 s16, s16, s15
	s_ashr_i32 s7, s6, 31
	s_lshl_b64 s[14:15], s[6:7], 2
	s_add_u32 s14, s18, s14
	s_addc_u32 s15, s16, s15
	v_lshl_add_u64 v[0:1], s[14:15], 0, v[96:97]
	v_lshl_add_u64 v[2:3], v[0:1], 0, v[60:61]
	global_load_dwordx4 v[116:119], v[2:3], off nt
	v_lshl_add_u64 v[2:3], v[0:1], 0, v[62:63]
	global_load_dwordx4 v[56:59], v[2:3], off nt
	v_lshl_add_u64 v[2:3], v[0:1], 0, v[64:65]
	global_load_dwordx4 v[52:55], v[2:3], off nt
	v_lshl_add_u64 v[2:3], v[0:1], 0, v[66:67]
	global_load_dwordx4 v[48:51], v[2:3], off nt
	v_lshl_add_u64 v[2:3], v[0:1], 0, v[68:69]
	global_load_dwordx4 v[44:47], v[2:3], off nt
	v_lshl_add_u64 v[2:3], v[0:1], 0, v[70:71]
	global_load_dwordx4 v[40:43], v[2:3], off nt
	v_lshl_add_u64 v[2:3], v[0:1], 0, v[72:73]
	global_load_dwordx4 v[36:39], v[2:3], off nt
	v_lshl_add_u64 v[2:3], v[0:1], 0, v[74:75]
	global_load_dwordx4 v[32:35], v[2:3], off nt
	v_lshl_add_u64 v[2:3], v[0:1], 0, v[76:77]
	global_load_dwordx4 v[28:31], v[2:3], off nt
	v_lshl_add_u64 v[2:3], v[0:1], 0, v[78:79]
	global_load_dwordx4 v[24:27], v[2:3], off nt
	v_lshl_add_u64 v[2:3], v[0:1], 0, v[80:81]
	global_load_dwordx4 v[20:23], v[2:3], off nt
	v_lshl_add_u64 v[2:3], v[0:1], 0, v[82:83]
	global_load_dwordx4 v[16:19], v[2:3], off nt
	v_lshl_add_u64 v[2:3], v[0:1], 0, v[84:85]
	global_load_dwordx4 v[12:15], v[2:3], off nt
	v_lshl_add_u64 v[2:3], v[0:1], 0, v[86:87]
	global_load_dwordx4 v[8:11], v[2:3], off nt
	v_lshl_add_u64 v[2:3], v[0:1], 0, v[88:89]
	global_load_dwordx4 v[4:7], v[2:3], off nt
	v_lshl_add_u64 v[0:1], v[0:1], 0, v[90:91]
	global_load_dwordx4 v[0:3], v[0:1], off nt
	v_add_u32_e32 v111, 0x410, v114
	s_lshl_b32 s7, s13, 7
	s_and_b32 s6, s6, 64
	s_or_b32 s6, s6, s7
	s_bitset1_b32 s6, 7
	s_ashr_i32 s7, s6, 31
	s_add_u32 s13, s21, s4
	s_addc_u32 s14, s22, s5
	s_lshl_b64 s[4:5], s[6:7], 12
	s_add_u32 s4, s13, s4
	s_addc_u32 s5, s14, s5
	s_lshl_b64 s[2:3], s[2:3], 1
	s_add_u32 s2, s4, s2
	s_addc_u32 s3, s5, s3
.Lcvp_4_skip:
	s_waitcnt lgkmcnt(0)
	ds_read2_b32 v[176:177], v113 offset0:65 offset1:73
	ds_read2_b32 v[178:179], v113 offset1:8
	ds_read2_b32 v[180:181], v113 offset0:130 offset1:138
	ds_read2_b32 v[182:183], v113 offset0:195 offset1:203
	v_lshl_add_u64 v[192:193], v[174:175], 0, v[92:93]
	s_waitcnt lgkmcnt(2)
	v_cvt_pk_bf16_f32 v170, v178, v176
	v_add_u32_e32 v176, 0x400, v113
	ds_read2_b32 v[184:185], v176 offset0:4 offset1:12
	ds_read2_b32 v[186:187], v176 offset0:69 offset1:77
	ds_read2_b32 v[188:189], v176 offset0:134 offset1:142
	ds_read2_b32 v[190:191], v176 offset0:199 offset1:207
	s_waitcnt lgkmcnt(4)
	v_cvt_pk_bf16_f32 v171, v180, v182
	v_lshl_add_u64 v[194:195], v[174:175], 0, v[98:99]
	s_waitcnt lgkmcnt(2)
	v_cvt_pk_bf16_f32 v172, v184, v186
	s_waitcnt lgkmcnt(0)
	v_cvt_pk_bf16_f32 v173, v188, v190
	global_store_dwordx4 v[192:193], v[170:173], off
	s_nop 1
	v_cvt_pk_bf16_f32 v170, v179, v177
	v_cvt_pk_bf16_f32 v171, v181, v183
	v_cvt_pk_bf16_f32 v172, v185, v187
	v_cvt_pk_bf16_f32 v173, v189, v191
	v_lshl_add_u64 v[178:179], v[174:175], 0, v[94:95]
	global_store_dwordx4 v[178:179], v[170:173], off
	ds_read2_b32 v[178:179], v113 offset0:81 offset1:89
	ds_read2_b32 v[180:181], v113 offset0:16 offset1:24
	ds_read2_b32 v[182:183], v113 offset0:146 offset1:154
	ds_read2_b32 v[184:185], v113 offset0:211 offset1:219
	ds_read2_b32 v[186:187], v176 offset0:20 offset1:28
	ds_read2_b32 v[188:189], v176 offset0:85 offset1:93
	ds_read2_b32 v[190:191], v176 offset0:150 offset1:158
	ds_read2_b32 v[192:193], v176 offset0:215 offset1:223
	s_waitcnt lgkmcnt(6)
	v_cvt_pk_bf16_f32 v170, v180, v178
	s_waitcnt lgkmcnt(4)
	v_cvt_pk_bf16_f32 v171, v182, v184
	s_waitcnt lgkmcnt(2)
	v_cvt_pk_bf16_f32 v172, v186, v188
	s_waitcnt lgkmcnt(0)
	v_cvt_pk_bf16_f32 v173, v190, v192
	global_store_dwordx4 v[194:195], v[170:173], off
	v_lshl_add_u64 v[194:195], v[174:175], 0, v[102:103]
	s_nop 0
	v_cvt_pk_bf16_f32 v170, v181, v179
	v_cvt_pk_bf16_f32 v171, v183, v185
	v_cvt_pk_bf16_f32 v172, v187, v189
	v_cvt_pk_bf16_f32 v173, v191, v193
	v_lshl_add_u64 v[178:179], v[174:175], 0, v[100:101]
	global_store_dwordx4 v[178:179], v[170:173], off
	ds_read2_b32 v[178:179], v113 offset0:32 offset1:40
	ds_read2_b32 v[180:181], v113 offset0:97 offset1:105
	ds_read2_b32 v[182:183], v113 offset0:162 offset1:170
	ds_read2_b32 v[184:185], v113 offset0:227 offset1:235
	ds_read2_b32 v[186:187], v176 offset0:36 offset1:44
	ds_read2_b32 v[188:189], v176 offset0:101 offset1:109
	ds_read2_b32 v[190:191], v176 offset0:166 offset1:174
	ds_read2_b32 v[192:193], v176 offset0:231 offset1:239
	s_waitcnt lgkmcnt(6)
	v_cvt_pk_bf16_f32 v170, v178, v180
	s_waitcnt lgkmcnt(4)
	v_cvt_pk_bf16_f32 v171, v182, v184
	s_waitcnt lgkmcnt(2)
	v_cvt_pk_bf16_f32 v172, v186, v188
	s_waitcnt lgkmcnt(0)
	v_cvt_pk_bf16_f32 v173, v190, v192
	global_store_dwordx4 v[194:195], v[170:173], off
	s_nop 1
	v_cvt_pk_bf16_f32 v170, v179, v181
	v_cvt_pk_bf16_f32 v171, v183, v185
	v_cvt_pk_bf16_f32 v172, v187, v189
	v_cvt_pk_bf16_f32 v173, v191, v193
	v_lshl_add_u64 v[178:179], v[174:175], 0, v[104:105]
	global_store_dwordx4 v[178:179], v[170:173], off
	ds_read2_b32 v[178:179], v113 offset0:48 offset1:56
	ds_read2_b32 v[180:181], v113 offset0:113 offset1:121
	ds_read2_b32 v[182:183], v113 offset0:178 offset1:186
	ds_read2_b32 v[184:185], v113 offset0:243 offset1:251
	ds_read2_b32 v[186:187], v176 offset0:52 offset1:60
	ds_read2_b32 v[188:189], v176 offset0:117 offset1:125
	ds_read2_b32 v[190:191], v176 offset0:182 offset1:190
	ds_read2_b32 v[176:177], v176 offset0:247 offset1:255
	v_lshl_add_u64 v[192:193], v[174:175], 0, v[106:107]
	s_waitcnt lgkmcnt(6)
	v_cvt_pk_bf16_f32 v170, v178, v180
	s_waitcnt lgkmcnt(4)
	v_cvt_pk_bf16_f32 v171, v182, v184
	s_waitcnt lgkmcnt(2)
	v_cvt_pk_bf16_f32 v172, v186, v188
	s_waitcnt lgkmcnt(0)
	v_cvt_pk_bf16_f32 v173, v190, v176
	global_store_dwordx4 v[192:193], v[170:173], off
	v_lshl_add_u64 v[174:175], v[174:175], 0, v[108:109]
	s_nop 0
	v_cvt_pk_bf16_f32 v170, v179, v181
	v_cvt_pk_bf16_f32 v171, v183, v185
	v_cvt_pk_bf16_f32 v172, v187, v189
	v_cvt_pk_bf16_f32 v173, v191, v177
	global_store_dwordx4 v[174:175], v[170:173], off
	s_waitcnt lgkmcnt(0)
	s_cmpk_lt_i32 s9, 0x1000
	s_cbranch_scc1 .Lcvp_4_loop

.LBB0_1167:
	s_ashr_i32 s4, s10, 31
	s_lshr_b32 s4, s4, 23
	s_add_i32 s5, s10, s4
	s_ashr_i32 s4, s5, 9
	s_and_b32 s5, s5, 0xfe00
	s_sub_i32 s5, s10, s5
	s_sext_i32_i16 s6, s5
	s_bfe_u32 s6, s6, 0x5001a
	s_add_i32 s6, s5, s6
	s_sext_i32_i16 s7, s6
	s_and_b32 s6, s6, 0xffe0
	s_sub_i32 s5, s5, s6
	s_sext_i32_i16 s5, s5
	s_lshl_b32 s6, s7, 1
	s_lshl_b32 s8, s5, 6
	s_ashr_i32 s5, s4, 31
	s_andn2_b32 s6, s6, 63
	s_lshl_b64 s[12:13], s[4:5], 23
	s_waitcnt lgkmcnt(0)
	s_add_u32 s9, s2, s12
	s_addc_u32 s11, s3, s13
	s_ashr_i32 s7, s6, 31
	s_lshl_b64 s[12:13], s[6:7], 13
	s_add_u32 s14, s9, s12
	s_addc_u32 s11, s11, s13
	s_ashr_i32 s9, s8, 31
	s_lshl_b64 s[12:13], s[8:9], 2
	s_add_u32 s12, s14, s12
	s_addc_u32 s13, s11, s13
	v_lshl_add_u64 v[0:1], s[12:13], 0, v[96:97]
	v_lshl_add_u64 v[2:3], v[0:1], 0, v[60:61]
	global_load_dwordx4 v[114:117], v[2:3], off nt
	v_lshl_add_u64 v[2:3], v[0:1], 0, v[62:63]
	global_load_dwordx4 v[56:59], v[2:3], off nt
	v_lshl_add_u64 v[2:3], v[0:1], 0, v[64:65]
	global_load_dwordx4 v[52:55], v[2:3], off nt
	v_lshl_add_u64 v[2:3], v[0:1], 0, v[66:67]
	global_load_dwordx4 v[48:51], v[2:3], off nt
	v_lshl_add_u64 v[2:3], v[0:1], 0, v[68:69]
	global_load_dwordx4 v[44:47], v[2:3], off nt
	v_lshl_add_u64 v[2:3], v[0:1], 0, v[70:71]
	global_load_dwordx4 v[40:43], v[2:3], off nt
	v_lshl_add_u64 v[2:3], v[0:1], 0, v[72:73]
	global_load_dwordx4 v[36:39], v[2:3], off nt
	v_lshl_add_u64 v[2:3], v[0:1], 0, v[74:75]
	global_load_dwordx4 v[32:35], v[2:3], off nt
	v_lshl_add_u64 v[2:3], v[0:1], 0, v[76:77]
	global_load_dwordx4 v[28:31], v[2:3], off nt
	v_lshl_add_u64 v[2:3], v[0:1], 0, v[78:79]
	global_load_dwordx4 v[24:27], v[2:3], off nt
	v_lshl_add_u64 v[2:3], v[0:1], 0, v[80:81]
	global_load_dwordx4 v[20:23], v[2:3], off nt
	v_lshl_add_u64 v[2:3], v[0:1], 0, v[82:83]
	global_load_dwordx4 v[16:19], v[2:3], off nt
	v_lshl_add_u64 v[2:3], v[0:1], 0, v[84:85]
	global_load_dwordx4 v[12:15], v[2:3], off nt
	v_lshl_add_u64 v[2:3], v[0:1], 0, v[86:87]
	global_load_dwordx4 v[8:11], v[2:3], off nt
	v_lshl_add_u64 v[2:3], v[0:1], 0, v[88:89]
	global_load_dwordx4 v[4:7], v[2:3], off nt
	v_lshl_add_u64 v[0:1], v[0:1], 0, v[90:91]
	global_load_dwordx4 v[0:3], v[0:1], off nt
	v_add_u32_e32 v111, 0x410, v113
	s_lshl_b64 s[4:5], s[4:5], 22
	s_add_u32 s11, s19, s4
	s_addc_u32 s12, s20, s5
	s_lshl_b64 s[4:5], s[8:9], 11
	s_add_u32 s8, s11, s4
	s_addc_u32 s9, s12, s5
	s_lshl_b64 s[4:5], s[6:7], 1
	s_add_u32 s4, s8, s4
	s_addc_u32 s5, s9, s5
.Lcvp_5_loop:
	s_waitcnt vmcnt(0) lgkmcnt(0)
	ds_write2_b32 v113, v114, v115 offset1:1
	ds_write2_b32 v113, v116, v117 offset0:2 offset1:3
	ds_write2_b32 v111, v56, v57 offset1:1
	v_add_u32_e32 v56, 0x418, v113
	ds_write2_b32 v56, v58, v59 offset1:1
	v_add_u32_e32 v56, 0x820, v113
	ds_write2_b32 v56, v52, v53 offset1:1
	v_add_u32_e32 v52, 0x828, v113
	ds_write2_b32 v52, v54, v55 offset1:1
	v_add_u32_e32 v52, 0xc30, v113
	ds_write2_b32 v52, v48, v49 offset1:1
	v_add_u32_e32 v48, 0xc38, v113
	ds_write2_b32 v48, v50, v51 offset1:1
	v_add_u32_e32 v48, 0x1040, v113
	ds_write2_b32 v48, v44, v45 offset1:1
	v_add_u32_e32 v44, 0x1048, v113
	ds_write2_b32 v44, v46, v47 offset1:1
	v_add_u32_e32 v44, 0x1450, v113
	ds_write2_b32 v44, v40, v41 offset1:1
	v_add_u32_e32 v40, 0x1458, v113
	ds_write2_b32 v40, v42, v43 offset1:1
	v_add_u32_e32 v40, 0x1860, v113
	ds_write2_b32 v40, v36, v37 offset1:1
	v_add_u32_e32 v36, 0x1868, v113
	ds_write2_b32 v36, v38, v39 offset1:1
	v_add_u32_e32 v36, 0x1c70, v113
	ds_write2_b32 v36, v32, v33 offset1:1
	v_add_u32_e32 v32, 0x1c78, v113
	ds_write2_b32 v32, v34, v35 offset1:1
	v_add_u32_e32 v32, 0x2080, v113
	ds_write2_b32 v32, v28, v29 offset1:1
	v_add_u32_e32 v28, 0x2088, v113
	ds_write2_b32 v28, v30, v31 offset1:1
	v_add_u32_e32 v28, 0x2490, v113
	ds_write2_b32 v28, v24, v25 offset1:1
	v_add_u32_e32 v24, 0x2498, v113
	ds_write2_b32 v24, v26, v27 offset1:1
	v_add_u32_e32 v24, 0x28a0, v113
	ds_write2_b32 v24, v20, v21 offset1:1
	v_add_u32_e32 v20, 0x28a8, v113
	ds_write2_b32 v20, v22, v23 offset1:1
	v_add_u32_e32 v20, 0x2cb0, v113
	ds_write2_b32 v20, v16, v17 offset1:1
	v_add_u32_e32 v16, 0x2cb8, v113
	ds_write2_b32 v16, v18, v19 offset1:1
	v_add_u32_e32 v16, 0x30c0, v113
	ds_write2_b32 v16, v12, v13 offset1:1
	v_add_u32_e32 v12, 0x30c8, v113
	ds_write2_b32 v12, v14, v15 offset1:1
	v_add_u32_e32 v12, 0x34d0, v113
	ds_write2_b32 v12, v8, v9 offset1:1
	v_add_u32_e32 v8, 0x34d8, v113
	ds_write2_b32 v8, v10, v11 offset1:1
	v_add_u32_e32 v8, 0x38e0, v113
	ds_write2_b32 v8, v4, v5 offset1:1
	v_add_u32_e32 v4, 0x38e8, v113
	ds_write2_b32 v4, v6, v7 offset1:1
	v_add_u32_e32 v4, 0x3cf0, v113
	ds_write2_b32 v4, v0, v1 offset1:1
	v_add_u32_e32 v0, 0x3cf8, v113
	ds_write2_b32 v0, v2, v3 offset1:1
	v_mov_b32_e32 v111, v97
	v_lshl_add_u64 v[174:175], s[4:5], 0, v[110:111]
	s_add_i32 s10, s10, s80
	s_cmpk_lt_i32 s10, 0x2000
	s_cbranch_scc0 .Lcvp_5_skip
	s_ashr_i32 s4, s10, 31
	s_lshr_b32 s4, s4, 23
	s_add_i32 s5, s10, s4
	s_ashr_i32 s4, s5, 9
	s_and_b32 s5, s5, 0xfe00
	s_sub_i32 s5, s10, s5
	s_sext_i32_i16 s6, s5
	s_bfe_u32 s6, s6, 0x5001a
	s_add_i32 s6, s5, s6
	s_sext_i32_i16 s7, s6
	s_and_b32 s6, s6, 0xffe0
	s_sub_i32 s5, s5, s6
	s_sext_i32_i16 s5, s5
	s_lshl_b32 s6, s7, 1
	s_lshl_b32 s8, s5, 6
	s_ashr_i32 s5, s4, 31
	s_andn2_b32 s6, s6, 63
	s_lshl_b64 s[12:13], s[4:5], 23
	s_waitcnt lgkmcnt(0)
	s_add_u32 s9, s2, s12
	s_addc_u32 s11, s3, s13
	s_ashr_i32 s7, s6, 31
	s_lshl_b64 s[12:13], s[6:7], 13
	s_add_u32 s14, s9, s12
	s_addc_u32 s11, s11, s13
	s_ashr_i32 s9, s8, 31
	s_lshl_b64 s[12:13], s[8:9], 2
	s_add_u32 s12, s14, s12
	s_addc_u32 s13, s11, s13
	v_lshl_add_u64 v[0:1], s[12:13], 0, v[96:97]
	v_lshl_add_u64 v[2:3], v[0:1], 0, v[60:61]
	global_load_dwordx4 v[114:117], v[2:3], off nt
	v_lshl_add_u64 v[2:3], v[0:1], 0, v[62:63]
	global_load_dwordx4 v[56:59], v[2:3], off nt
	v_lshl_add_u64 v[2:3], v[0:1], 0, v[64:65]
	global_load_dwordx4 v[52:55], v[2:3], off nt
	v_lshl_add_u64 v[2:3], v[0:1], 0, v[66:67]
	global_load_dwordx4 v[48:51], v[2:3], off nt
	v_lshl_add_u64 v[2:3], v[0:1], 0, v[68:69]
	global_load_dwordx4 v[44:47], v[2:3], off nt
	v_lshl_add_u64 v[2:3], v[0:1], 0, v[70:71]
	global_load_dwordx4 v[40:43], v[2:3], off nt
	v_lshl_add_u64 v[2:3], v[0:1], 0, v[72:73]
	global_load_dwordx4 v[36:39], v[2:3], off nt
	v_lshl_add_u64 v[2:3], v[0:1], 0, v[74:75]
	global_load_dwordx4 v[32:35], v[2:3], off nt
	v_lshl_add_u64 v[2:3], v[0:1], 0, v[76:77]
	global_load_dwordx4 v[28:31], v[2:3], off nt
	v_lshl_add_u64 v[2:3], v[0:1], 0, v[78:79]
	global_load_dwordx4 v[24:27], v[2:3], off nt
	v_lshl_add_u64 v[2:3], v[0:1], 0, v[80:81]
	global_load_dwordx4 v[20:23], v[2:3], off nt
	v_lshl_add_u64 v[2:3], v[0:1], 0, v[82:83]
	global_load_dwordx4 v[16:19], v[2:3], off nt
	v_lshl_add_u64 v[2:3], v[0:1], 0, v[84:85]
	global_load_dwordx4 v[12:15], v[2:3], off nt
	v_lshl_add_u64 v[2:3], v[0:1], 0, v[86:87]
	global_load_dwordx4 v[8:11], v[2:3], off nt
	v_lshl_add_u64 v[2:3], v[0:1], 0, v[88:89]
	global_load_dwordx4 v[4:7], v[2:3], off nt
	v_lshl_add_u64 v[0:1], v[0:1], 0, v[90:91]
	global_load_dwordx4 v[0:3], v[0:1], off nt
	v_add_u32_e32 v111, 0x410, v113
	s_lshl_b64 s[4:5], s[4:5], 22
	s_add_u32 s11, s19, s4
	s_addc_u32 s12, s20, s5
	s_lshl_b64 s[4:5], s[8:9], 11
	s_add_u32 s8, s11, s4
	s_addc_u32 s9, s12, s5
	s_lshl_b64 s[4:5], s[6:7], 1
	s_add_u32 s4, s8, s4
	s_addc_u32 s5, s9, s5
.Lcvp_5_skip:
	s_waitcnt lgkmcnt(0)
	ds_read2_b32 v[176:177], v112 offset0:65 offset1:73
	ds_read2_b32 v[178:179], v112 offset1:8
	ds_read2_b32 v[180:181], v112 offset0:130 offset1:138
	ds_read2_b32 v[182:183], v112 offset0:195 offset1:203
	v_lshl_add_u64 v[192:193], v[174:175], 0, v[92:93]
	s_waitcnt lgkmcnt(2)
	v_cvt_pk_bf16_f32 v170, v178, v176
	v_add_u32_e32 v176, 0x400, v112
	ds_read2_b32 v[184:185], v176 offset0:4 offset1:12
	ds_read2_b32 v[186:187], v176 offset0:69 offset1:77
	ds_read2_b32 v[188:189], v176 offset0:134 offset1:142
	ds_read2_b32 v[190:191], v176 offset0:199 offset1:207
	s_waitcnt lgkmcnt(4)
	v_cvt_pk_bf16_f32 v171, v180, v182
	v_lshl_add_u64 v[194:195], v[174:175], 0, v[98:99]
	s_waitcnt lgkmcnt(2)
	v_cvt_pk_bf16_f32 v172, v184, v186
	s_waitcnt lgkmcnt(0)
	v_cvt_pk_bf16_f32 v173, v188, v190
	global_store_dwordx4 v[192:193], v[170:173], off
	s_nop 1
	v_cvt_pk_bf16_f32 v170, v179, v177
	v_cvt_pk_bf16_f32 v171, v181, v183
	v_cvt_pk_bf16_f32 v172, v185, v187
	v_cvt_pk_bf16_f32 v173, v189, v191
	v_lshl_add_u64 v[178:179], v[174:175], 0, v[94:95]
	global_store_dwordx4 v[178:179], v[170:173], off
	ds_read2_b32 v[178:179], v112 offset0:81 offset1:89
	ds_read2_b32 v[180:181], v112 offset0:16 offset1:24
	ds_read2_b32 v[182:183], v112 offset0:146 offset1:154
	ds_read2_b32 v[184:185], v112 offset0:211 offset1:219
	ds_read2_b32 v[186:187], v176 offset0:20 offset1:28
	ds_read2_b32 v[188:189], v176 offset0:85 offset1:93
	ds_read2_b32 v[190:191], v176 offset0:150 offset1:158
	ds_read2_b32 v[192:193], v176 offset0:215 offset1:223
	s_waitcnt lgkmcnt(6)
	v_cvt_pk_bf16_f32 v170, v180, v178
	s_waitcnt lgkmcnt(4)
	v_cvt_pk_bf16_f32 v171, v182, v184
	s_waitcnt lgkmcnt(2)
	v_cvt_pk_bf16_f32 v172, v186, v188
	s_waitcnt lgkmcnt(0)
	v_cvt_pk_bf16_f32 v173, v190, v192
	global_store_dwordx4 v[194:195], v[170:173], off
	v_lshl_add_u64 v[194:195], v[174:175], 0, v[102:103]
	s_nop 0
	v_cvt_pk_bf16_f32 v170, v181, v179
	v_cvt_pk_bf16_f32 v171, v183, v185
	v_cvt_pk_bf16_f32 v172, v187, v189
	v_cvt_pk_bf16_f32 v173, v191, v193
	v_lshl_add_u64 v[178:179], v[174:175], 0, v[100:101]
	global_store_dwordx4 v[178:179], v[170:173], off
	ds_read2_b32 v[178:179], v112 offset0:32 offset1:40
	ds_read2_b32 v[180:181], v112 offset0:97 offset1:105
	ds_read2_b32 v[182:183], v112 offset0:162 offset1:170
	ds_read2_b32 v[184:185], v112 offset0:227 offset1:235
	ds_read2_b32 v[186:187], v176 offset0:36 offset1:44
	ds_read2_b32 v[188:189], v176 offset0:101 offset1:109
	ds_read2_b32 v[190:191], v176 offset0:166 offset1:174
	ds_read2_b32 v[192:193], v176 offset0:231 offset1:239
	s_waitcnt lgkmcnt(6)
	v_cvt_pk_bf16_f32 v170, v178, v180
	s_waitcnt lgkmcnt(4)
	v_cvt_pk_bf16_f32 v171, v182, v184
	s_waitcnt lgkmcnt(2)
	v_cvt_pk_bf16_f32 v172, v186, v188
	s_waitcnt lgkmcnt(0)
	v_cvt_pk_bf16_f32 v173, v190, v192
	global_store_dwordx4 v[194:195], v[170:173], off
	s_nop 1
	v_cvt_pk_bf16_f32 v170, v179, v181
	v_cvt_pk_bf16_f32 v171, v183, v185
	v_cvt_pk_bf16_f32 v172, v187, v189
	v_cvt_pk_bf16_f32 v173, v191, v193
	v_lshl_add_u64 v[178:179], v[174:175], 0, v[104:105]
	global_store_dwordx4 v[178:179], v[170:173], off
	ds_read2_b32 v[178:179], v112 offset0:48 offset1:56
	ds_read2_b32 v[180:181], v112 offset0:113 offset1:121
	ds_read2_b32 v[182:183], v112 offset0:178 offset1:186
	ds_read2_b32 v[184:185], v112 offset0:243 offset1:251
	ds_read2_b32 v[186:187], v176 offset0:52 offset1:60
	ds_read2_b32 v[188:189], v176 offset0:117 offset1:125
	ds_read2_b32 v[190:191], v176 offset0:182 offset1:190
	ds_read2_b32 v[176:177], v176 offset0:247 offset1:255
	v_lshl_add_u64 v[192:193], v[174:175], 0, v[106:107]
	s_waitcnt lgkmcnt(6)
	v_cvt_pk_bf16_f32 v170, v178, v180
	s_waitcnt lgkmcnt(4)
	v_cvt_pk_bf16_f32 v171, v182, v184
	s_waitcnt lgkmcnt(2)
	v_cvt_pk_bf16_f32 v172, v186, v188
	s_waitcnt lgkmcnt(0)
	v_cvt_pk_bf16_f32 v173, v190, v176
	global_store_dwordx4 v[192:193], v[170:173], off
	v_lshl_add_u64 v[174:175], v[174:175], 0, v[108:109]
	s_nop 0
	v_cvt_pk_bf16_f32 v170, v179, v181
	v_cvt_pk_bf16_f32 v171, v183, v185
	v_cvt_pk_bf16_f32 v172, v187, v189
	v_cvt_pk_bf16_f32 v173, v191, v177
	global_store_dwordx4 v[174:175], v[170:173], off
	s_waitcnt lgkmcnt(0)
	s_cmpk_lt_i32 s10, 0x2000
	s_cbranch_scc1 .Lcvp_5_loop

.LBB0_1536:
	s_ashr_i32 s2, s8, 31
	s_lshr_b32 s2, s2, 23
	s_add_i32 s2, s8, s2
	s_ashr_i32 s4, s2, 9
	s_and_b32 s2, s2, 0xfe00
	s_sub_i32 s2, s8, s2
	s_sext_i32_i16 s3, s2
	s_bfe_u32 s3, s3, 0x4001b
	s_add_i32 s3, s2, s3
	s_sext_i32_i16 s5, s3
	s_and_b32 s3, s3, 0xfff0
	s_sub_i32 s2, s2, s3
	s_sext_i32_i16 s11, s2
	s_lshl_b32 s2, s5, 2
	s_ashr_i32 s5, s4, 31
	s_andn2_b32 s2, s2, 63
	s_lshl_b32 s6, s11, 6
	s_lshl_b64 s[4:5], s[4:5], 23
	s_add_u32 s7, s9, s4
	s_addc_u32 s14, s10, s5
	s_ashr_i32 s3, s2, 31
	s_lshl_b64 s[12:13], s[2:3], 12
	s_add_u32 s15, s7, s12
	s_addc_u32 s14, s14, s13
	s_ashr_i32 s7, s6, 31
	s_lshl_b64 s[12:13], s[6:7], 2
	s_add_u32 s12, s15, s12
	s_addc_u32 s13, s14, s13
	v_lshl_add_u64 v[0:1], s[12:13], 0, v[96:97]
	v_lshl_add_u64 v[2:3], v[0:1], 0, v[60:61]
	global_load_dwordx4 v[114:117], v[2:3], off nt
	v_lshl_add_u64 v[2:3], v[0:1], 0, v[62:63]
	global_load_dwordx4 v[56:59], v[2:3], off nt
	v_lshl_add_u64 v[2:3], v[0:1], 0, v[64:65]
	global_load_dwordx4 v[52:55], v[2:3], off nt
	v_lshl_add_u64 v[2:3], v[0:1], 0, v[66:67]
	global_load_dwordx4 v[48:51], v[2:3], off nt
	v_lshl_add_u64 v[2:3], v[0:1], 0, v[68:69]
	global_load_dwordx4 v[44:47], v[2:3], off nt
	v_lshl_add_u64 v[2:3], v[0:1], 0, v[70:71]
	global_load_dwordx4 v[40:43], v[2:3], off nt
	v_lshl_add_u64 v[2:3], v[0:1], 0, v[72:73]
	global_load_dwordx4 v[36:39], v[2:3], off nt
	v_lshl_add_u64 v[2:3], v[0:1], 0, v[74:75]
	global_load_dwordx4 v[32:35], v[2:3], off nt
	v_lshl_add_u64 v[2:3], v[0:1], 0, v[76:77]
	global_load_dwordx4 v[28:31], v[2:3], off nt
	v_lshl_add_u64 v[2:3], v[0:1], 0, v[78:79]
	global_load_dwordx4 v[24:27], v[2:3], off nt
	v_lshl_add_u64 v[2:3], v[0:1], 0, v[80:81]
	global_load_dwordx4 v[20:23], v[2:3], off nt
	v_lshl_add_u64 v[2:3], v[0:1], 0, v[82:83]
	global_load_dwordx4 v[16:19], v[2:3], off nt
	v_lshl_add_u64 v[2:3], v[0:1], 0, v[84:85]
	global_load_dwordx4 v[12:15], v[2:3], off nt
	v_lshl_add_u64 v[2:3], v[0:1], 0, v[86:87]
	global_load_dwordx4 v[8:11], v[2:3], off nt
	v_lshl_add_u64 v[2:3], v[0:1], 0, v[88:89]
	global_load_dwordx4 v[4:7], v[2:3], off nt
	v_lshl_add_u64 v[0:1], v[0:1], 0, v[90:91]
	global_load_dwordx4 v[0:3], v[0:1], off nt
	v_add_u32_e32 v111, 0x410, v113
	s_lshl_b32 s7, s11, 7
	s_and_b32 s7, s7, 0xffffff00
	s_and_b32 s6, s6, 64
	s_or_b32 s6, s7, s6
	s_ashr_i32 s7, s6, 31
	s_add_u32 s11, s16, s4
	s_addc_u32 s12, s18, s5
	s_lshl_b64 s[4:5], s[6:7], 12
	s_add_u32 s4, s11, s4
	s_addc_u32 s5, s12, s5
	s_lshl_b64 s[2:3], s[2:3], 1
	s_add_u32 s2, s4, s2
	s_addc_u32 s3, s5, s3
.Lcvp_6_loop:
	s_waitcnt vmcnt(0) lgkmcnt(0)
	ds_write2_b32 v113, v114, v115 offset1:1
	ds_write2_b32 v113, v116, v117 offset0:2 offset1:3
	ds_write2_b32 v111, v56, v57 offset1:1
	v_add_u32_e32 v56, 0x418, v113
	ds_write2_b32 v56, v58, v59 offset1:1
	v_add_u32_e32 v56, 0x820, v113
	ds_write2_b32 v56, v52, v53 offset1:1
	v_add_u32_e32 v52, 0x828, v113
	ds_write2_b32 v52, v54, v55 offset1:1
	v_add_u32_e32 v52, 0xc30, v113
	ds_write2_b32 v52, v48, v49 offset1:1
	v_add_u32_e32 v48, 0xc38, v113
	ds_write2_b32 v48, v50, v51 offset1:1
	v_add_u32_e32 v48, 0x1040, v113
	ds_write2_b32 v48, v44, v45 offset1:1
	v_add_u32_e32 v44, 0x1048, v113
	ds_write2_b32 v44, v46, v47 offset1:1
	v_add_u32_e32 v44, 0x1450, v113
	ds_write2_b32 v44, v40, v41 offset1:1
	v_add_u32_e32 v40, 0x1458, v113
	ds_write2_b32 v40, v42, v43 offset1:1
	v_add_u32_e32 v40, 0x1860, v113
	ds_write2_b32 v40, v36, v37 offset1:1
	v_add_u32_e32 v36, 0x1868, v113
	ds_write2_b32 v36, v38, v39 offset1:1
	v_add_u32_e32 v36, 0x1c70, v113
	ds_write2_b32 v36, v32, v33 offset1:1
	v_add_u32_e32 v32, 0x1c78, v113
	ds_write2_b32 v32, v34, v35 offset1:1
	v_add_u32_e32 v32, 0x2080, v113
	ds_write2_b32 v32, v28, v29 offset1:1
	v_add_u32_e32 v28, 0x2088, v113
	ds_write2_b32 v28, v30, v31 offset1:1
	v_add_u32_e32 v28, 0x2490, v113
	ds_write2_b32 v28, v24, v25 offset1:1
	v_add_u32_e32 v24, 0x2498, v113
	ds_write2_b32 v24, v26, v27 offset1:1
	v_add_u32_e32 v24, 0x28a0, v113
	ds_write2_b32 v24, v20, v21 offset1:1
	v_add_u32_e32 v20, 0x28a8, v113
	ds_write2_b32 v20, v22, v23 offset1:1
	v_add_u32_e32 v20, 0x2cb0, v113
	ds_write2_b32 v20, v16, v17 offset1:1
	v_add_u32_e32 v16, 0x2cb8, v113
	ds_write2_b32 v16, v18, v19 offset1:1
	v_add_u32_e32 v16, 0x30c0, v113
	ds_write2_b32 v16, v12, v13 offset1:1
	v_add_u32_e32 v12, 0x30c8, v113
	ds_write2_b32 v12, v14, v15 offset1:1
	v_add_u32_e32 v12, 0x34d0, v113
	ds_write2_b32 v12, v8, v9 offset1:1
	v_add_u32_e32 v8, 0x34d8, v113
	ds_write2_b32 v8, v10, v11 offset1:1
	v_add_u32_e32 v8, 0x38e0, v113
	ds_write2_b32 v8, v4, v5 offset1:1
	v_add_u32_e32 v4, 0x38e8, v113
	ds_write2_b32 v4, v6, v7 offset1:1
	v_add_u32_e32 v4, 0x3cf0, v113
	ds_write2_b32 v4, v0, v1 offset1:1
	v_add_u32_e32 v0, 0x3cf8, v113
	ds_write2_b32 v0, v2, v3 offset1:1
	v_mov_b32_e32 v111, v97
	v_lshl_add_u64 v[174:175], s[2:3], 0, v[110:111]
	s_add_i32 s8, s8, s80
	s_cmpk_lt_i32 s8, 0x2000
	s_cbranch_scc0 .Lcvp_6_skip
	s_ashr_i32 s2, s8, 31
	s_lshr_b32 s2, s2, 23
	s_add_i32 s2, s8, s2
	s_ashr_i32 s4, s2, 9
	s_and_b32 s2, s2, 0xfe00
	s_sub_i32 s2, s8, s2
	s_sext_i32_i16 s3, s2
	s_bfe_u32 s3, s3, 0x4001b
	s_add_i32 s3, s2, s3
	s_sext_i32_i16 s5, s3
	s_and_b32 s3, s3, 0xfff0
	s_sub_i32 s2, s2, s3
	s_sext_i32_i16 s11, s2
	s_lshl_b32 s2, s5, 2
	s_ashr_i32 s5, s4, 31
	s_andn2_b32 s2, s2, 63
	s_lshl_b32 s6, s11, 6
	s_lshl_b64 s[4:5], s[4:5], 23
	s_add_u32 s7, s9, s4
	s_addc_u32 s14, s10, s5
	s_ashr_i32 s3, s2, 31
	s_lshl_b64 s[12:13], s[2:3], 12
	s_add_u32 s15, s7, s12
	s_addc_u32 s14, s14, s13
	s_ashr_i32 s7, s6, 31
	s_lshl_b64 s[12:13], s[6:7], 2
	s_add_u32 s12, s15, s12
	s_addc_u32 s13, s14, s13
	v_lshl_add_u64 v[0:1], s[12:13], 0, v[96:97]
	v_lshl_add_u64 v[2:3], v[0:1], 0, v[60:61]
	global_load_dwordx4 v[114:117], v[2:3], off nt
	v_lshl_add_u64 v[2:3], v[0:1], 0, v[62:63]
	global_load_dwordx4 v[56:59], v[2:3], off nt
	v_lshl_add_u64 v[2:3], v[0:1], 0, v[64:65]
	global_load_dwordx4 v[52:55], v[2:3], off nt
	v_lshl_add_u64 v[2:3], v[0:1], 0, v[66:67]
	global_load_dwordx4 v[48:51], v[2:3], off nt
	v_lshl_add_u64 v[2:3], v[0:1], 0, v[68:69]
	global_load_dwordx4 v[44:47], v[2:3], off nt
	v_lshl_add_u64 v[2:3], v[0:1], 0, v[70:71]
	global_load_dwordx4 v[40:43], v[2:3], off nt
	v_lshl_add_u64 v[2:3], v[0:1], 0, v[72:73]
	global_load_dwordx4 v[36:39], v[2:3], off nt
	v_lshl_add_u64 v[2:3], v[0:1], 0, v[74:75]
	global_load_dwordx4 v[32:35], v[2:3], off nt
	v_lshl_add_u64 v[2:3], v[0:1], 0, v[76:77]
	global_load_dwordx4 v[28:31], v[2:3], off nt
	v_lshl_add_u64 v[2:3], v[0:1], 0, v[78:79]
	global_load_dwordx4 v[24:27], v[2:3], off nt
	v_lshl_add_u64 v[2:3], v[0:1], 0, v[80:81]
	global_load_dwordx4 v[20:23], v[2:3], off nt
	v_lshl_add_u64 v[2:3], v[0:1], 0, v[82:83]
	global_load_dwordx4 v[16:19], v[2:3], off nt
	v_lshl_add_u64 v[2:3], v[0:1], 0, v[84:85]
	global_load_dwordx4 v[12:15], v[2:3], off nt
	v_lshl_add_u64 v[2:3], v[0:1], 0, v[86:87]
	global_load_dwordx4 v[8:11], v[2:3], off nt
	v_lshl_add_u64 v[2:3], v[0:1], 0, v[88:89]
	global_load_dwordx4 v[4:7], v[2:3], off nt
	v_lshl_add_u64 v[0:1], v[0:1], 0, v[90:91]
	global_load_dwordx4 v[0:3], v[0:1], off nt
	v_add_u32_e32 v111, 0x410, v113
	s_lshl_b32 s7, s11, 7
	s_and_b32 s7, s7, 0xffffff00
	s_and_b32 s6, s6, 64
	s_or_b32 s6, s7, s6
	s_ashr_i32 s7, s6, 31
	s_add_u32 s11, s16, s4
	s_addc_u32 s12, s18, s5
	s_lshl_b64 s[4:5], s[6:7], 12
	s_add_u32 s4, s11, s4
	s_addc_u32 s5, s12, s5
	s_lshl_b64 s[2:3], s[2:3], 1
	s_add_u32 s2, s4, s2
	s_addc_u32 s3, s5, s3
.Lcvp_6_skip:
	s_waitcnt lgkmcnt(0)
	ds_read2_b32 v[176:177], v112 offset0:65 offset1:73
	ds_read2_b32 v[178:179], v112 offset1:8
	ds_read2_b32 v[180:181], v112 offset0:130 offset1:138
	ds_read2_b32 v[182:183], v112 offset0:195 offset1:203
	v_lshl_add_u64 v[192:193], v[174:175], 0, v[92:93]
	s_waitcnt lgkmcnt(2)
	v_cvt_pk_bf16_f32 v170, v178, v176
	v_add_u32_e32 v176, 0x400, v112
	ds_read2_b32 v[184:185], v176 offset0:4 offset1:12
	ds_read2_b32 v[186:187], v176 offset0:69 offset1:77
	ds_read2_b32 v[188:189], v176 offset0:134 offset1:142
	ds_read2_b32 v[190:191], v176 offset0:199 offset1:207
	s_waitcnt lgkmcnt(4)
	v_cvt_pk_bf16_f32 v171, v180, v182
	v_lshl_add_u64 v[194:195], v[174:175], 0, v[98:99]
	s_waitcnt lgkmcnt(2)
	v_cvt_pk_bf16_f32 v172, v184, v186
	s_waitcnt lgkmcnt(0)
	v_cvt_pk_bf16_f32 v173, v188, v190
	global_store_dwordx4 v[192:193], v[170:173], off
	s_nop 1
	v_cvt_pk_bf16_f32 v170, v179, v177
	v_cvt_pk_bf16_f32 v171, v181, v183
	v_cvt_pk_bf16_f32 v172, v185, v187
	v_cvt_pk_bf16_f32 v173, v189, v191
	v_lshl_add_u64 v[178:179], v[174:175], 0, v[94:95]
	global_store_dwordx4 v[178:179], v[170:173], off
	ds_read2_b32 v[178:179], v112 offset0:81 offset1:89
	ds_read2_b32 v[180:181], v112 offset0:16 offset1:24
	ds_read2_b32 v[182:183], v112 offset0:146 offset1:154
	ds_read2_b32 v[184:185], v112 offset0:211 offset1:219
	ds_read2_b32 v[186:187], v176 offset0:20 offset1:28
	ds_read2_b32 v[188:189], v176 offset0:85 offset1:93
	ds_read2_b32 v[190:191], v176 offset0:150 offset1:158
	ds_read2_b32 v[192:193], v176 offset0:215 offset1:223
	s_waitcnt lgkmcnt(6)
	v_cvt_pk_bf16_f32 v170, v180, v178
	s_waitcnt lgkmcnt(4)
	v_cvt_pk_bf16_f32 v171, v182, v184
	s_waitcnt lgkmcnt(2)
	v_cvt_pk_bf16_f32 v172, v186, v188
	s_waitcnt lgkmcnt(0)
	v_cvt_pk_bf16_f32 v173, v190, v192
	global_store_dwordx4 v[194:195], v[170:173], off
	v_lshl_add_u64 v[194:195], v[174:175], 0, v[102:103]
	s_nop 0
	v_cvt_pk_bf16_f32 v170, v181, v179
	v_cvt_pk_bf16_f32 v171, v183, v185
	v_cvt_pk_bf16_f32 v172, v187, v189
	v_cvt_pk_bf16_f32 v173, v191, v193
	v_lshl_add_u64 v[178:179], v[174:175], 0, v[100:101]
	global_store_dwordx4 v[178:179], v[170:173], off
	ds_read2_b32 v[178:179], v112 offset0:32 offset1:40
	ds_read2_b32 v[180:181], v112 offset0:97 offset1:105
	ds_read2_b32 v[182:183], v112 offset0:162 offset1:170
	ds_read2_b32 v[184:185], v112 offset0:227 offset1:235
	ds_read2_b32 v[186:187], v176 offset0:36 offset1:44
	ds_read2_b32 v[188:189], v176 offset0:101 offset1:109
	ds_read2_b32 v[190:191], v176 offset0:166 offset1:174
	ds_read2_b32 v[192:193], v176 offset0:231 offset1:239
	s_waitcnt lgkmcnt(6)
	v_cvt_pk_bf16_f32 v170, v178, v180
	s_waitcnt lgkmcnt(4)
	v_cvt_pk_bf16_f32 v171, v182, v184
	s_waitcnt lgkmcnt(2)
	v_cvt_pk_bf16_f32 v172, v186, v188
	s_waitcnt lgkmcnt(0)
	v_cvt_pk_bf16_f32 v173, v190, v192
	global_store_dwordx4 v[194:195], v[170:173], off
	s_nop 1
	v_cvt_pk_bf16_f32 v170, v179, v181
	v_cvt_pk_bf16_f32 v171, v183, v185
	v_cvt_pk_bf16_f32 v172, v187, v189
	v_cvt_pk_bf16_f32 v173, v191, v193
	v_lshl_add_u64 v[178:179], v[174:175], 0, v[104:105]
	global_store_dwordx4 v[178:179], v[170:173], off
	ds_read2_b32 v[178:179], v112 offset0:48 offset1:56
	ds_read2_b32 v[180:181], v112 offset0:113 offset1:121
	ds_read2_b32 v[182:183], v112 offset0:178 offset1:186
	ds_read2_b32 v[184:185], v112 offset0:243 offset1:251
	ds_read2_b32 v[186:187], v176 offset0:52 offset1:60
	ds_read2_b32 v[188:189], v176 offset0:117 offset1:125
	ds_read2_b32 v[190:191], v176 offset0:182 offset1:190
	ds_read2_b32 v[176:177], v176 offset0:247 offset1:255
	v_lshl_add_u64 v[192:193], v[174:175], 0, v[106:107]
	s_waitcnt lgkmcnt(6)
	v_cvt_pk_bf16_f32 v170, v178, v180
	s_waitcnt lgkmcnt(4)
	v_cvt_pk_bf16_f32 v171, v182, v184
	s_waitcnt lgkmcnt(2)
	v_cvt_pk_bf16_f32 v172, v186, v188
	s_waitcnt lgkmcnt(0)
	v_cvt_pk_bf16_f32 v173, v190, v176
	global_store_dwordx4 v[192:193], v[170:173], off
	v_lshl_add_u64 v[174:175], v[174:175], 0, v[108:109]
	s_nop 0
	v_cvt_pk_bf16_f32 v170, v179, v181
	v_cvt_pk_bf16_f32 v171, v183, v185
	v_cvt_pk_bf16_f32 v172, v187, v189
	v_cvt_pk_bf16_f32 v173, v191, v177
	global_store_dwordx4 v[174:175], v[170:173], off
	s_waitcnt lgkmcnt(0)
	s_cmpk_lt_i32 s8, 0x2000
	s_cbranch_scc1 .Lcvp_6_loop

.LBB0_1613:
	s_ashr_i32 s2, s8, 31
	s_lshr_b32 s2, s2, 23
	s_add_i32 s3, s8, s2
	s_ashr_i32 s2, s3, 9
	s_and_b32 s3, s3, 0xfe00
	s_sub_i32 s3, s8, s3
	s_sext_i32_i16 s4, s3
	s_bfe_u32 s4, s4, 0x5001a
	s_add_i32 s4, s3, s4
	s_sext_i32_i16 s5, s4
	s_and_b32 s4, s4, 0xffe0
	s_sub_i32 s3, s3, s4
	s_sext_i32_i16 s3, s3
	s_lshl_b32 s4, s5, 1
	s_lshl_b32 s6, s3, 6
	s_ashr_i32 s3, s2, 31
	s_andn2_b32 s4, s4, 63
	s_lshl_b64 s[12:13], s[2:3], 23
	s_add_u32 s7, s9, s12
	s_addc_u32 s11, s10, s13
	s_ashr_i32 s5, s4, 31
	s_lshl_b64 s[12:13], s[4:5], 13
	s_add_u32 s14, s7, s12
	s_addc_u32 s11, s11, s13
	s_ashr_i32 s7, s6, 31
	s_lshl_b64 s[12:13], s[6:7], 2
	s_add_u32 s12, s14, s12
	s_addc_u32 s13, s11, s13
	v_lshl_add_u64 v[0:1], s[12:13], 0, v[96:97]
	v_lshl_add_u64 v[2:3], v[0:1], 0, v[60:61]
	global_load_dwordx4 v[114:117], v[2:3], off nt
	v_lshl_add_u64 v[2:3], v[0:1], 0, v[62:63]
	global_load_dwordx4 v[56:59], v[2:3], off nt
	v_lshl_add_u64 v[2:3], v[0:1], 0, v[64:65]
	global_load_dwordx4 v[52:55], v[2:3], off nt
	v_lshl_add_u64 v[2:3], v[0:1], 0, v[66:67]
	global_load_dwordx4 v[48:51], v[2:3], off nt
	v_lshl_add_u64 v[2:3], v[0:1], 0, v[68:69]
	global_load_dwordx4 v[44:47], v[2:3], off nt
	v_lshl_add_u64 v[2:3], v[0:1], 0, v[70:71]
	global_load_dwordx4 v[40:43], v[2:3], off nt
	v_lshl_add_u64 v[2:3], v[0:1], 0, v[72:73]
	global_load_dwordx4 v[36:39], v[2:3], off nt
	v_lshl_add_u64 v[2:3], v[0:1], 0, v[74:75]
	global_load_dwordx4 v[32:35], v[2:3], off nt
	v_lshl_add_u64 v[2:3], v[0:1], 0, v[76:77]
	global_load_dwordx4 v[28:31], v[2:3], off nt
	v_lshl_add_u64 v[2:3], v[0:1], 0, v[78:79]
	global_load_dwordx4 v[24:27], v[2:3], off nt
	v_lshl_add_u64 v[2:3], v[0:1], 0, v[80:81]
	global_load_dwordx4 v[20:23], v[2:3], off nt
	v_lshl_add_u64 v[2:3], v[0:1], 0, v[82:83]
	global_load_dwordx4 v[16:19], v[2:3], off nt
	v_lshl_add_u64 v[2:3], v[0:1], 0, v[84:85]
	global_load_dwordx4 v[12:15], v[2:3], off nt
	v_lshl_add_u64 v[2:3], v[0:1], 0, v[86:87]
	global_load_dwordx4 v[8:11], v[2:3], off nt
	v_lshl_add_u64 v[2:3], v[0:1], 0, v[88:89]
	global_load_dwordx4 v[4:7], v[2:3], off nt
	v_lshl_add_u64 v[0:1], v[0:1], 0, v[90:91]
	global_load_dwordx4 v[0:3], v[0:1], off nt
	v_add_u32_e32 v111, 0x410, v113
	s_lshl_b64 s[2:3], s[2:3], 22
	s_add_u32 s11, s15, s2
	s_addc_u32 s12, s16, s3
	s_lshl_b64 s[2:3], s[6:7], 11
	s_add_u32 s6, s11, s2
	s_addc_u32 s7, s12, s3
	s_lshl_b64 s[2:3], s[4:5], 1
	s_add_u32 s2, s6, s2
	s_addc_u32 s3, s7, s3
.Lcvp_7_loop:
	s_waitcnt vmcnt(0) lgkmcnt(0)
	ds_write2_b32 v113, v114, v115 offset1:1
	ds_write2_b32 v113, v116, v117 offset0:2 offset1:3
	ds_write2_b32 v111, v56, v57 offset1:1
	v_add_u32_e32 v56, 0x418, v113
	ds_write2_b32 v56, v58, v59 offset1:1
	v_add_u32_e32 v56, 0x820, v113
	ds_write2_b32 v56, v52, v53 offset1:1
	v_add_u32_e32 v52, 0x828, v113
	ds_write2_b32 v52, v54, v55 offset1:1
	v_add_u32_e32 v52, 0xc30, v113
	ds_write2_b32 v52, v48, v49 offset1:1
	v_add_u32_e32 v48, 0xc38, v113
	ds_write2_b32 v48, v50, v51 offset1:1
	v_add_u32_e32 v48, 0x1040, v113
	ds_write2_b32 v48, v44, v45 offset1:1
	v_add_u32_e32 v44, 0x1048, v113
	ds_write2_b32 v44, v46, v47 offset1:1
	v_add_u32_e32 v44, 0x1450, v113
	ds_write2_b32 v44, v40, v41 offset1:1
	v_add_u32_e32 v40, 0x1458, v113
	ds_write2_b32 v40, v42, v43 offset1:1
	v_add_u32_e32 v40, 0x1860, v113
	ds_write2_b32 v40, v36, v37 offset1:1
	v_add_u32_e32 v36, 0x1868, v113
	ds_write2_b32 v36, v38, v39 offset1:1
	v_add_u32_e32 v36, 0x1c70, v113
	ds_write2_b32 v36, v32, v33 offset1:1
	v_add_u32_e32 v32, 0x1c78, v113
	ds_write2_b32 v32, v34, v35 offset1:1
	v_add_u32_e32 v32, 0x2080, v113
	ds_write2_b32 v32, v28, v29 offset1:1
	v_add_u32_e32 v28, 0x2088, v113
	ds_write2_b32 v28, v30, v31 offset1:1
	v_add_u32_e32 v28, 0x2490, v113
	ds_write2_b32 v28, v24, v25 offset1:1
	v_add_u32_e32 v24, 0x2498, v113
	ds_write2_b32 v24, v26, v27 offset1:1
	v_add_u32_e32 v24, 0x28a0, v113
	ds_write2_b32 v24, v20, v21 offset1:1
	v_add_u32_e32 v20, 0x28a8, v113
	ds_write2_b32 v20, v22, v23 offset1:1
	v_add_u32_e32 v20, 0x2cb0, v113
	ds_write2_b32 v20, v16, v17 offset1:1
	v_add_u32_e32 v16, 0x2cb8, v113
	ds_write2_b32 v16, v18, v19 offset1:1
	v_add_u32_e32 v16, 0x30c0, v113
	ds_write2_b32 v16, v12, v13 offset1:1
	v_add_u32_e32 v12, 0x30c8, v113
	ds_write2_b32 v12, v14, v15 offset1:1
	v_add_u32_e32 v12, 0x34d0, v113
	ds_write2_b32 v12, v8, v9 offset1:1
	v_add_u32_e32 v8, 0x34d8, v113
	ds_write2_b32 v8, v10, v11 offset1:1
	v_add_u32_e32 v8, 0x38e0, v113
	ds_write2_b32 v8, v4, v5 offset1:1
	v_add_u32_e32 v4, 0x38e8, v113
	ds_write2_b32 v4, v6, v7 offset1:1
	v_add_u32_e32 v4, 0x3cf0, v113
	ds_write2_b32 v4, v0, v1 offset1:1
	v_add_u32_e32 v0, 0x3cf8, v113
	ds_write2_b32 v0, v2, v3 offset1:1
	v_mov_b32_e32 v111, v97
	v_lshl_add_u64 v[174:175], s[2:3], 0, v[110:111]
	s_add_i32 s8, s8, s80
	s_cmpk_lt_i32 s8, 0x2000
	s_cbranch_scc0 .Lcvp_7_skip
	s_ashr_i32 s2, s8, 31
	s_lshr_b32 s2, s2, 23
	s_add_i32 s3, s8, s2
	s_ashr_i32 s2, s3, 9
	s_and_b32 s3, s3, 0xfe00
	s_sub_i32 s3, s8, s3
	s_sext_i32_i16 s4, s3
	s_bfe_u32 s4, s4, 0x5001a
	s_add_i32 s4, s3, s4
	s_sext_i32_i16 s5, s4
	s_and_b32 s4, s4, 0xffe0
	s_sub_i32 s3, s3, s4
	s_sext_i32_i16 s3, s3
	s_lshl_b32 s4, s5, 1
	s_lshl_b32 s6, s3, 6
	s_ashr_i32 s3, s2, 31
	s_andn2_b32 s4, s4, 63
	s_lshl_b64 s[12:13], s[2:3], 23
	s_add_u32 s7, s9, s12
	s_addc_u32 s11, s10, s13
	s_ashr_i32 s5, s4, 31
	s_lshl_b64 s[12:13], s[4:5], 13
	s_add_u32 s14, s7, s12
	s_addc_u32 s11, s11, s13
	s_ashr_i32 s7, s6, 31
	s_lshl_b64 s[12:13], s[6:7], 2
	s_add_u32 s12, s14, s12
	s_addc_u32 s13, s11, s13
	v_lshl_add_u64 v[0:1], s[12:13], 0, v[96:97]
	v_lshl_add_u64 v[2:3], v[0:1], 0, v[60:61]
	global_load_dwordx4 v[114:117], v[2:3], off nt
	v_lshl_add_u64 v[2:3], v[0:1], 0, v[62:63]
	global_load_dwordx4 v[56:59], v[2:3], off nt
	v_lshl_add_u64 v[2:3], v[0:1], 0, v[64:65]
	global_load_dwordx4 v[52:55], v[2:3], off nt
	v_lshl_add_u64 v[2:3], v[0:1], 0, v[66:67]
	global_load_dwordx4 v[48:51], v[2:3], off nt
	v_lshl_add_u64 v[2:3], v[0:1], 0, v[68:69]
	global_load_dwordx4 v[44:47], v[2:3], off nt
	v_lshl_add_u64 v[2:3], v[0:1], 0, v[70:71]
	global_load_dwordx4 v[40:43], v[2:3], off nt
	v_lshl_add_u64 v[2:3], v[0:1], 0, v[72:73]
	global_load_dwordx4 v[36:39], v[2:3], off nt
	v_lshl_add_u64 v[2:3], v[0:1], 0, v[74:75]
	global_load_dwordx4 v[32:35], v[2:3], off nt
	v_lshl_add_u64 v[2:3], v[0:1], 0, v[76:77]
	global_load_dwordx4 v[28:31], v[2:3], off nt
	v_lshl_add_u64 v[2:3], v[0:1], 0, v[78:79]
	global_load_dwordx4 v[24:27], v[2:3], off nt
	v_lshl_add_u64 v[2:3], v[0:1], 0, v[80:81]
	global_load_dwordx4 v[20:23], v[2:3], off nt
	v_lshl_add_u64 v[2:3], v[0:1], 0, v[82:83]
	global_load_dwordx4 v[16:19], v[2:3], off nt
	v_lshl_add_u64 v[2:3], v[0:1], 0, v[84:85]
	global_load_dwordx4 v[12:15], v[2:3], off nt
	v_lshl_add_u64 v[2:3], v[0:1], 0, v[86:87]
	global_load_dwordx4 v[8:11], v[2:3], off nt
	v_lshl_add_u64 v[2:3], v[0:1], 0, v[88:89]
	global_load_dwordx4 v[4:7], v[2:3], off nt
	v_lshl_add_u64 v[0:1], v[0:1], 0, v[90:91]
	global_load_dwordx4 v[0:3], v[0:1], off nt
	v_add_u32_e32 v111, 0x410, v113
	s_lshl_b64 s[2:3], s[2:3], 22
	s_add_u32 s11, s15, s2
	s_addc_u32 s12, s16, s3
	s_lshl_b64 s[2:3], s[6:7], 11
	s_add_u32 s6, s11, s2
	s_addc_u32 s7, s12, s3
	s_lshl_b64 s[2:3], s[4:5], 1
	s_add_u32 s2, s6, s2
	s_addc_u32 s3, s7, s3
